# speedup vs baseline: 1.0160x; 1.0160x over previous
.Lk4_st1_6:
	s_add_u32 s52, s10, 0x800000
	s_addc_u32 s53, s11, 0
	v_lshlrev_b32_e32 v169, 2, v98
	v_lshlrev_b32_e32 v170, 2, v100
	global_load_dwordx4 v[128:131], v169, s[52:53] nt
	global_load_dwordx4 v[132:135], v170, s[52:53] nt
	s_add_u32 s52, s10, 0xc00000
	s_addc_u32 s53, s11, 0
	v_lshlrev_b32_e32 v169, 2, v94
	v_lshlrev_b32_e32 v170, 2, v96
	global_load_dwordx4 v[172:175], v169, s[52:53] nt
	global_load_dwordx4 v[176:179], v170, s[52:53] nt
	v_mfma_f32_16x16x32_f16 a[0:3], v[70:73], v[82:85], a[0:3]
	ds_read_b128 v[14:17], v144
	v_mfma_f32_16x16x32_f16 a[4:7], v[70:73], v[86:89], a[4:7]
	ds_read_b128 v[18:21], v146
	v_mfma_f32_16x16x32_f16 a[12:15], v[66:69], v[82:85], a[12:15]
	ds_read_b128 v[42:45], v166
	v_mfma_f32_16x16x32_f16 a[16:19], v[66:69], v[86:89], a[16:19]
	ds_read_b128 v[38:41], v166 offset:1024
	v_mfma_f32_16x16x32_f16 a[28:31], v[58:61], v[82:85], a[28:31]
	ds_read_b128 v[34:37], v166 offset:2048
	v_mfma_f32_16x16x32_f16 a[60:63], v[58:61], v[86:89], a[60:63]
	ds_read_b128 v[30:33], v166 offset:3072
	v_mfma_f32_16x16x32_f16 a[8:11], v[54:57], v[82:85], a[8:11]
	ds_read_b128 v[26:29], v166 offset:4096
	v_mfma_f32_16x16x32_f16 a[20:23], v[54:57], v[86:89], a[20:23]
	ds_read_b128 v[22:25], v166 offset:5120
	v_mfma_f32_16x16x32_f16 a[24:27], v[46:49], v[82:85], a[24:27]
	ds_read_b128 v[10:13], v166 offset:6144
	v_mfma_f32_16x16x32_f16 a[36:39], v[46:49], v[86:89], a[36:39]
	ds_read_b128 v[6:9], v166 offset:7168
	v_mfma_f32_16x16x32_f16 a[44:47], v[50:53], v[82:85], a[44:47]
	ds_read_b128 v[2:5], v166 offset:8192
	v_mfma_f32_16x16x32_f16 a[64:67], v[50:53], v[86:89], a[64:67]
	v_mfma_f32_16x16x32_f16 a[32:35], v[62:65], v[82:85], a[32:35]
	v_mfma_f32_16x16x32_f16 a[40:43], v[62:65], v[86:89], a[40:43]
	v_mfma_f32_16x16x32_f16 a[48:51], v[74:77], v[82:85], a[48:51]
	v_mfma_f32_16x16x32_f16 a[52:55], v[74:77], v[86:89], a[52:55]
	v_mfma_f32_16x16x32_f16 a[56:59], v[78:81], v[82:85], a[56:59]
	v_mfma_f32_16x16x32_f16 a[68:71], v[78:81], v[86:89], a[68:71]
	s_waitcnt lgkmcnt(8)
	v_mfma_f32_16x16x32_f16 a[0:3], v[42:45], v[14:17], a[0:3]
	ds_read_b128 v[82:85], v145
	v_mfma_f32_16x16x32_f16 a[4:7], v[42:45], v[18:21], a[4:7]
	ds_read_b128 v[86:89], v147
	s_waitcnt lgkmcnt(9)
	v_mfma_f32_16x16x32_f16 a[12:15], v[38:41], v[14:17], a[12:15]
	ds_read_b128 v[70:73], v166 offset:9216
	v_mfma_f32_16x16x32_f16 a[16:19], v[38:41], v[18:21], a[16:19]
	ds_read_b128 v[66:69], v166 offset:10240
	s_waitcnt lgkmcnt(10)
	v_mfma_f32_16x16x32_f16 a[28:31], v[34:37], v[14:17], a[28:31]
	ds_read_b128 v[58:61], v166 offset:11264
	v_mfma_f32_16x16x32_f16 a[60:63], v[34:37], v[18:21], a[60:63]
	ds_read_b128 v[54:57], v166 offset:12288
	s_waitcnt lgkmcnt(11)
	v_mfma_f32_16x16x32_f16 a[8:11], v[30:33], v[14:17], a[8:11]
	ds_read_b128 v[46:49], v166 offset:13312
	v_mfma_f32_16x16x32_f16 a[20:23], v[30:33], v[18:21], a[20:23]
	ds_read_b128 v[50:53], v166 offset:14336
	s_waitcnt lgkmcnt(12)
	v_mfma_f32_16x16x32_f16 a[24:27], v[26:29], v[14:17], a[24:27]
	ds_read_b128 v[62:65], v166 offset:15360
	v_mfma_f32_16x16x32_f16 a[36:39], v[26:29], v[18:21], a[36:39]
	ds_read_b128 v[74:77], v166 offset:16384
	s_waitcnt lgkmcnt(13)
	v_mfma_f32_16x16x32_f16 a[44:47], v[22:25], v[14:17], a[44:47]
	ds_read_b128 v[78:81], v166 offset:17408
	v_mfma_f32_16x16x32_f16 a[64:67], v[22:25], v[18:21], a[64:67]
	s_waitcnt lgkmcnt(13)
	v_mfma_f32_16x16x32_f16 a[32:35], v[10:13], v[14:17], a[32:35]
	v_mfma_f32_16x16x32_f16 a[40:43], v[10:13], v[18:21], a[40:43]
	s_waitcnt lgkmcnt(12)
	v_mfma_f32_16x16x32_f16 a[48:51], v[6:9], v[14:17], a[48:51]
	v_mfma_f32_16x16x32_f16 a[52:55], v[6:9], v[18:21], a[52:55]
	s_waitcnt lgkmcnt(11)
	v_mfma_f32_16x16x32_f16 a[56:59], v[2:5], v[14:17], a[56:59]
	v_mfma_f32_16x16x32_f16 a[68:71], v[2:5], v[18:21], a[68:71]
	s_waitcnt lgkmcnt(8)
	v_mfma_f32_16x16x32_f16 a[0:3], v[70:73], v[82:85], a[0:3]
	ds_read_b128 v[14:17], v148
	v_mfma_f32_16x16x32_f16 a[4:7], v[70:73], v[86:89], a[4:7]
	ds_read_b128 v[18:21], v150
	s_waitcnt lgkmcnt(9)
	v_mfma_f32_16x16x32_f16 a[12:15], v[66:69], v[82:85], a[12:15]
	ds_read_b128 v[42:45], v167
	v_mfma_f32_16x16x32_f16 a[16:19], v[66:69], v[86:89], a[16:19]
	ds_read_b128 v[38:41], v167 offset:1024
	s_waitcnt lgkmcnt(10)
	v_mfma_f32_16x16x32_f16 a[28:31], v[58:61], v[82:85], a[28:31]
	ds_read_b128 v[34:37], v167 offset:2048
	v_mfma_f32_16x16x32_f16 a[60:63], v[58:61], v[86:89], a[60:63]
	ds_read_b128 v[30:33], v167 offset:3072
	s_waitcnt lgkmcnt(11)
	v_mfma_f32_16x16x32_f16 a[8:11], v[54:57], v[82:85], a[8:11]
	ds_read_b128 v[26:29], v167 offset:4096
	v_mfma_f32_16x16x32_f16 a[20:23], v[54:57], v[86:89], a[20:23]
	ds_read_b128 v[22:25], v167 offset:5120
	s_waitcnt lgkmcnt(12)
	v_mfma_f32_16x16x32_f16 a[24:27], v[46:49], v[82:85], a[24:27]
	ds_read_b128 v[10:13], v167 offset:6144
	v_mfma_f32_16x16x32_f16 a[36:39], v[46:49], v[86:89], a[36:39]
	ds_read_b128 v[6:9], v167 offset:7168
	s_waitcnt lgkmcnt(13)
	v_mfma_f32_16x16x32_f16 a[44:47], v[50:53], v[82:85], a[44:47]
	ds_read_b128 v[2:5], v167 offset:8192
	v_mfma_f32_16x16x32_f16 a[64:67], v[50:53], v[86:89], a[64:67]
	s_waitcnt lgkmcnt(13)
	v_mfma_f32_16x16x32_f16 a[32:35], v[62:65], v[82:85], a[32:35]
	v_mfma_f32_16x16x32_f16 a[40:43], v[62:65], v[86:89], a[40:43]
	s_waitcnt lgkmcnt(12)
	v_mfma_f32_16x16x32_f16 a[48:51], v[74:77], v[82:85], a[48:51]
	v_mfma_f32_16x16x32_f16 a[52:55], v[74:77], v[86:89], a[52:55]
	s_waitcnt lgkmcnt(11)
	v_mfma_f32_16x16x32_f16 a[56:59], v[78:81], v[82:85], a[56:59]
	v_mfma_f32_16x16x32_f16 a[68:71], v[78:81], v[86:89], a[68:71]
	s_waitcnt lgkmcnt(8)
	v_mfma_f32_16x16x32_f16 a[0:3], v[42:45], v[14:17], a[0:3]
	ds_read_b128 v[82:85], v149
	v_mfma_f32_16x16x32_f16 a[4:7], v[42:45], v[18:21], a[4:7]
	ds_read_b128 v[86:89], v151
	s_waitcnt lgkmcnt(9)
	v_mfma_f32_16x16x32_f16 a[12:15], v[38:41], v[14:17], a[12:15]
	ds_read_b128 v[70:73], v167 offset:9216
	v_mfma_f32_16x16x32_f16 a[16:19], v[38:41], v[18:21], a[16:19]
	ds_read_b128 v[66:69], v167 offset:10240
	s_waitcnt lgkmcnt(10)
	v_mfma_f32_16x16x32_f16 a[28:31], v[34:37], v[14:17], a[28:31]
	ds_read_b128 v[58:61], v167 offset:11264
	v_mfma_f32_16x16x32_f16 a[60:63], v[34:37], v[18:21], a[60:63]
	ds_read_b128 v[54:57], v167 offset:12288
	s_waitcnt lgkmcnt(11)
	v_mfma_f32_16x16x32_f16 a[8:11], v[30:33], v[14:17], a[8:11]
	ds_read_b128 v[46:49], v167 offset:13312
	v_mfma_f32_16x16x32_f16 a[20:23], v[30:33], v[18:21], a[20:23]
	ds_read_b128 v[50:53], v167 offset:14336
	s_waitcnt lgkmcnt(12)
	v_mfma_f32_16x16x32_f16 a[24:27], v[26:29], v[14:17], a[24:27]
	ds_read_b128 v[62:65], v167 offset:15360
	v_mfma_f32_16x16x32_f16 a[36:39], v[26:29], v[18:21], a[36:39]
	ds_read_b128 v[74:77], v167 offset:16384
	s_waitcnt lgkmcnt(13)
	v_mfma_f32_16x16x32_f16 a[44:47], v[22:25], v[14:17], a[44:47]
	ds_read_b128 v[78:81], v167 offset:17408
	v_mfma_f32_16x16x32_f16 a[64:67], v[22:25], v[18:21], a[64:67]
	s_waitcnt lgkmcnt(13)
	v_mfma_f32_16x16x32_f16 a[32:35], v[10:13], v[14:17], a[32:35]
	v_mfma_f32_16x16x32_f16 a[40:43], v[10:13], v[18:21], a[40:43]
	s_waitcnt lgkmcnt(12)
	v_mfma_f32_16x16x32_f16 a[48:51], v[6:9], v[14:17], a[48:51]
	v_mfma_f32_16x16x32_f16 a[52:55], v[6:9], v[18:21], a[52:55]
	s_waitcnt lgkmcnt(11)
	v_mfma_f32_16x16x32_f16 a[56:59], v[2:5], v[14:17], a[56:59]
	v_mfma_f32_16x16x32_f16 a[68:71], v[2:5], v[18:21], a[68:71]
	s_waitcnt lgkmcnt(8)
	v_mfma_f32_16x16x32_f16 a[0:3], v[70:73], v[82:85], a[0:3]
	ds_read_b128 v[14:17], v150
	v_mfma_f32_16x16x32_f16 a[4:7], v[70:73], v[86:89], a[4:7]
	ds_read_b128 v[18:21], v152
	s_waitcnt lgkmcnt(9)
	v_mfma_f32_16x16x32_f16 a[12:15], v[66:69], v[82:85], a[12:15]
	ds_read_b128 v[42:45], v168
	v_mfma_f32_16x16x32_f16 a[16:19], v[66:69], v[86:89], a[16:19]
	ds_read_b128 v[38:41], v168 offset:1024
	s_waitcnt lgkmcnt(10)
	v_mfma_f32_16x16x32_f16 a[28:31], v[58:61], v[82:85], a[28:31]
	ds_read_b128 v[34:37], v168 offset:2048
	v_mfma_f32_16x16x32_f16 a[60:63], v[58:61], v[86:89], a[60:63]
	ds_read_b128 v[30:33], v168 offset:3072
	s_waitcnt lgkmcnt(11)
	v_mfma_f32_16x16x32_f16 a[8:11], v[54:57], v[82:85], a[8:11]
	ds_read_b128 v[26:29], v168 offset:4096
	v_mfma_f32_16x16x32_f16 a[20:23], v[54:57], v[86:89], a[20:23]
	ds_read_b128 v[22:25], v168 offset:5120
	s_waitcnt lgkmcnt(12)
	v_mfma_f32_16x16x32_f16 a[24:27], v[46:49], v[82:85], a[24:27]
	ds_read_b128 v[10:13], v168 offset:6144
	v_mfma_f32_16x16x32_f16 a[36:39], v[46:49], v[86:89], a[36:39]
	ds_read_b128 v[6:9], v168 offset:7168
	s_waitcnt lgkmcnt(13)
	v_mfma_f32_16x16x32_f16 a[44:47], v[50:53], v[82:85], a[44:47]
	ds_read_b128 v[2:5], v168 offset:8192
	v_mfma_f32_16x16x32_f16 a[64:67], v[50:53], v[86:89], a[64:67]
	s_waitcnt lgkmcnt(13)
	v_mfma_f32_16x16x32_f16 a[32:35], v[62:65], v[82:85], a[32:35]
	v_mfma_f32_16x16x32_f16 a[40:43], v[62:65], v[86:89], a[40:43]
	s_waitcnt lgkmcnt(12)
	v_mfma_f32_16x16x32_f16 a[48:51], v[74:77], v[82:85], a[48:51]
	v_mfma_f32_16x16x32_f16 a[52:55], v[74:77], v[86:89], a[52:55]
	s_waitcnt lgkmcnt(11)
	v_mfma_f32_16x16x32_f16 a[56:59], v[78:81], v[82:85], a[56:59]
	v_mfma_f32_16x16x32_f16 a[68:71], v[78:81], v[86:89], a[68:71]
	s_waitcnt lgkmcnt(8)
	v_mfma_f32_16x16x32_f16 a[0:3], v[42:45], v[14:17], a[0:3]
	ds_read_b128 v[82:85], v151
	v_mfma_f32_16x16x32_f16 a[4:7], v[42:45], v[18:21], a[4:7]
	ds_read_b128 v[86:89], v153
	s_waitcnt lgkmcnt(9)
	v_mfma_f32_16x16x32_f16 a[12:15], v[38:41], v[14:17], a[12:15]
	ds_read_b128 v[70:73], v168 offset:9216
	v_mfma_f32_16x16x32_f16 a[16:19], v[38:41], v[18:21], a[16:19]
	ds_read_b128 v[66:69], v168 offset:10240
	s_waitcnt lgkmcnt(10)
	v_mfma_f32_16x16x32_f16 a[28:31], v[34:37], v[14:17], a[28:31]
	ds_read_b128 v[58:61], v168 offset:11264
	v_mfma_f32_16x16x32_f16 a[60:63], v[34:37], v[18:21], a[60:63]
	ds_read_b128 v[54:57], v168 offset:12288
	s_waitcnt lgkmcnt(11)
	v_mfma_f32_16x16x32_f16 a[8:11], v[30:33], v[14:17], a[8:11]
	ds_read_b128 v[46:49], v168 offset:13312
	v_mfma_f32_16x16x32_f16 a[20:23], v[30:33], v[18:21], a[20:23]
	ds_read_b128 v[50:53], v168 offset:14336
	s_waitcnt lgkmcnt(12)
	v_mfma_f32_16x16x32_f16 a[24:27], v[26:29], v[14:17], a[24:27]
	ds_read_b128 v[62:65], v168 offset:15360
	v_mfma_f32_16x16x32_f16 a[36:39], v[26:29], v[18:21], a[36:39]
	ds_read_b128 v[74:77], v168 offset:16384
	s_waitcnt lgkmcnt(13)
	v_mfma_f32_16x16x32_f16 a[44:47], v[22:25], v[14:17], a[44:47]
	ds_read_b128 v[78:81], v168 offset:17408
	v_mfma_f32_16x16x32_f16 a[64:67], v[22:25], v[18:21], a[64:67]
	s_waitcnt lgkmcnt(13)
	v_mfma_f32_16x16x32_f16 a[32:35], v[10:13], v[14:17], a[32:35]
	v_mfma_f32_16x16x32_f16 a[40:43], v[10:13], v[18:21], a[40:43]
	s_waitcnt lgkmcnt(12)
	v_mfma_f32_16x16x32_f16 a[48:51], v[6:9], v[14:17], a[48:51]
	v_mfma_f32_16x16x32_f16 a[52:55], v[6:9], v[18:21], a[52:55]
	s_waitcnt lgkmcnt(11)
	v_mfma_f32_16x16x32_f16 a[56:59], v[2:5], v[14:17], a[56:59]
	v_mfma_f32_16x16x32_f16 a[68:71], v[2:5], v[18:21], a[68:71]
	s_waitcnt vmcnt(4) lgkmcnt(0)
	s_barrier
	s_add_u32 s52, s50, 0x1f800
	s_addc_u32 s53, s51, 0
	s_add_i32 m0, s42, 0x1f000
	s_nop 0
	global_load_lds_dwordx4 v137, s[52:53]
	s_add_i32 m0, s43, 0x1f000
	s_nop 0
	global_load_lds_dwordx4 v138, s[52:53]
	s_cmp_lt_u32 s42, 0x800
	s_cbranch_scc0 .Lk4_st4_7
	s_add_i32 m0, s44, 0x1f000
	s_nop 0
	global_load_lds_dwordx4 v139, s[52:53]
.Lk4_st4_7:
	v_add_u32_e32 v169, s17, v118
	s_nop 1
	v_readfirstlane_b32 s14, v169
	s_mov_b32 m0, s14
	s_nop 0
	global_load_lds_dwordx4 v[102:103], off nt
	v_add_u32_e32 v169, s17, v90
	s_nop 1
	v_readfirstlane_b32 s14, v169
	s_mov_b32 m0, s14
	s_nop 0
	global_load_lds_dwordx4 v[104:105], off nt
	v_add_u32_e32 v169, s17, v91
	s_nop 1
	v_readfirstlane_b32 s14, v169
	s_mov_b32 m0, s14
	s_nop 0
	global_load_lds_dwordx4 v[108:109], off nt
	v_add_u32_e32 v169, s17, v119
	s_nop 1
	v_readfirstlane_b32 s14, v169
	s_mov_b32 m0, s14
	s_nop 0
	global_load_lds_dwordx4 v[112:113], off nt
	s_add_u32 s52, s10, 0xc00000
	s_addc_u32 s53, s11, 0
	v_lshlrev_b32_e32 v169, 2, v98
	v_lshlrev_b32_e32 v170, 2, v100
	global_load_dwordx4 v[140:143], v169, s[52:53] nt
	global_load_dwordx4 v[144:147], v170, s[52:53] nt
	v_mfma_f32_16x16x32_f16 a[0:3], v[70:73], v[82:85], a[0:3]
	ds_read_b128 v[14:17], v152
	v_mfma_f32_16x16x32_f16 a[4:7], v[70:73], v[86:89], a[4:7]
	ds_read_b128 v[18:21], v154
	v_mfma_f32_16x16x32_f16 a[12:15], v[66:69], v[82:85], a[12:15]
	ds_read_b128 v[42:45], v164
	v_mfma_f32_16x16x32_f16 a[16:19], v[66:69], v[86:89], a[16:19]
	ds_read_b128 v[38:41], v164 offset:1024
	v_mfma_f32_16x16x32_f16 a[28:31], v[58:61], v[82:85], a[28:31]
	ds_read_b128 v[34:37], v164 offset:2048
	v_mfma_f32_16x16x32_f16 a[60:63], v[58:61], v[86:89], a[60:63]
	ds_read_b128 v[30:33], v164 offset:3072
	v_mfma_f32_16x16x32_f16 a[8:11], v[54:57], v[82:85], a[8:11]
	ds_read_b128 v[26:29], v164 offset:4096
	v_mfma_f32_16x16x32_f16 a[20:23], v[54:57], v[86:89], a[20:23]
	ds_read_b128 v[22:25], v164 offset:5120
	v_mfma_f32_16x16x32_f16 a[24:27], v[46:49], v[82:85], a[24:27]
	ds_read_b128 v[10:13], v164 offset:6144
	v_mfma_f32_16x16x32_f16 a[36:39], v[46:49], v[86:89], a[36:39]
	ds_read_b128 v[6:9], v164 offset:7168
	v_mfma_f32_16x16x32_f16 a[44:47], v[50:53], v[82:85], a[44:47]
	ds_read_b128 v[2:5], v164 offset:8192
	v_mfma_f32_16x16x32_f16 a[64:67], v[50:53], v[86:89], a[64:67]
	v_mfma_f32_16x16x32_f16 a[32:35], v[62:65], v[82:85], a[32:35]
	v_mfma_f32_16x16x32_f16 a[40:43], v[62:65], v[86:89], a[40:43]
	v_mfma_f32_16x16x32_f16 a[48:51], v[74:77], v[82:85], a[48:51]
	v_mfma_f32_16x16x32_f16 a[52:55], v[74:77], v[86:89], a[52:55]
	v_mfma_f32_16x16x32_f16 a[56:59], v[78:81], v[82:85], a[56:59]
	v_mfma_f32_16x16x32_f16 a[68:71], v[78:81], v[86:89], a[68:71]
	s_waitcnt lgkmcnt(8)
	v_mfma_f32_16x16x32_f16 a[0:3], v[42:45], v[14:17], a[0:3]
	ds_read_b128 v[82:85], v153
	v_mfma_f32_16x16x32_f16 a[4:7], v[42:45], v[18:21], a[4:7]
	ds_read_b128 v[86:89], v155
	s_waitcnt lgkmcnt(9)
	v_mfma_f32_16x16x32_f16 a[12:15], v[38:41], v[14:17], a[12:15]
	ds_read_b128 v[70:73], v164 offset:9216
	v_mfma_f32_16x16x32_f16 a[16:19], v[38:41], v[18:21], a[16:19]
	ds_read_b128 v[66:69], v164 offset:10240
	s_waitcnt lgkmcnt(10)
	v_mfma_f32_16x16x32_f16 a[28:31], v[34:37], v[14:17], a[28:31]
	ds_read_b128 v[58:61], v164 offset:11264
	v_mfma_f32_16x16x32_f16 a[60:63], v[34:37], v[18:21], a[60:63]
	ds_read_b128 v[54:57], v164 offset:12288
	s_waitcnt lgkmcnt(11)
	v_mfma_f32_16x16x32_f16 a[8:11], v[30:33], v[14:17], a[8:11]
	ds_read_b128 v[46:49], v164 offset:13312
	v_mfma_f32_16x16x32_f16 a[20:23], v[30:33], v[18:21], a[20:23]
	ds_read_b128 v[50:53], v164 offset:14336
	s_waitcnt lgkmcnt(12)
	v_mfma_f32_16x16x32_f16 a[24:27], v[26:29], v[14:17], a[24:27]
	ds_read_b128 v[62:65], v164 offset:15360
	v_mfma_f32_16x16x32_f16 a[36:39], v[26:29], v[18:21], a[36:39]
	ds_read_b128 v[74:77], v164 offset:16384
	s_waitcnt lgkmcnt(13)
	v_mfma_f32_16x16x32_f16 a[44:47], v[22:25], v[14:17], a[44:47]
	ds_read_b128 v[78:81], v164 offset:17408
	v_mfma_f32_16x16x32_f16 a[64:67], v[22:25], v[18:21], a[64:67]
	s_waitcnt lgkmcnt(13)
	v_mfma_f32_16x16x32_f16 a[32:35], v[10:13], v[14:17], a[32:35]
	v_mfma_f32_16x16x32_f16 a[40:43], v[10:13], v[18:21], a[40:43]
	s_waitcnt lgkmcnt(12)
	v_mfma_f32_16x16x32_f16 a[48:51], v[6:9], v[14:17], a[48:51]
	v_mfma_f32_16x16x32_f16 a[52:55], v[6:9], v[18:21], a[52:55]
	s_waitcnt lgkmcnt(11)
	v_mfma_f32_16x16x32_f16 a[56:59], v[2:5], v[14:17], a[56:59]
	v_mfma_f32_16x16x32_f16 a[68:71], v[2:5], v[18:21], a[68:71]
	s_waitcnt lgkmcnt(8)
	v_mfma_f32_16x16x32_f16 a[0:3], v[70:73], v[82:85], a[0:3]
	ds_read_b128 v[14:17], v156
	v_mfma_f32_16x16x32_f16 a[4:7], v[70:73], v[86:89], a[4:7]
	ds_read_b128 v[18:21], v158
	s_waitcnt lgkmcnt(9)
	v_mfma_f32_16x16x32_f16 a[12:15], v[66:69], v[82:85], a[12:15]
	ds_read_b128 v[42:45], v165
	v_mfma_f32_16x16x32_f16 a[16:19], v[66:69], v[86:89], a[16:19]
	ds_read_b128 v[38:41], v165 offset:1024
	s_waitcnt lgkmcnt(10)
	v_mfma_f32_16x16x32_f16 a[28:31], v[58:61], v[82:85], a[28:31]
	ds_read_b128 v[34:37], v165 offset:2048
	v_mfma_f32_16x16x32_f16 a[60:63], v[58:61], v[86:89], a[60:63]
	ds_read_b128 v[30:33], v165 offset:3072
	s_waitcnt lgkmcnt(11)
	v_mfma_f32_16x16x32_f16 a[8:11], v[54:57], v[82:85], a[8:11]
	ds_read_b128 v[26:29], v165 offset:4096
	v_mfma_f32_16x16x32_f16 a[20:23], v[54:57], v[86:89], a[20:23]
	ds_read_b128 v[22:25], v165 offset:5120
	s_waitcnt lgkmcnt(12)
	v_mfma_f32_16x16x32_f16 a[24:27], v[46:49], v[82:85], a[24:27]
	ds_read_b128 v[10:13], v165 offset:6144
	v_mfma_f32_16x16x32_f16 a[36:39], v[46:49], v[86:89], a[36:39]
	ds_read_b128 v[6:9], v165 offset:7168
	s_waitcnt lgkmcnt(13)
	v_mfma_f32_16x16x32_f16 a[44:47], v[50:53], v[82:85], a[44:47]
	ds_read_b128 v[2:5], v165 offset:8192
	v_mfma_f32_16x16x32_f16 a[64:67], v[50:53], v[86:89], a[64:67]
	s_waitcnt lgkmcnt(13)
	v_mfma_f32_16x16x32_f16 a[32:35], v[62:65], v[82:85], a[32:35]
	v_mfma_f32_16x16x32_f16 a[40:43], v[62:65], v[86:89], a[40:43]
	s_waitcnt lgkmcnt(12)
	v_mfma_f32_16x16x32_f16 a[48:51], v[74:77], v[82:85], a[48:51]
	v_mfma_f32_16x16x32_f16 a[52:55], v[74:77], v[86:89], a[52:55]
	s_waitcnt lgkmcnt(11)
	v_mfma_f32_16x16x32_f16 a[56:59], v[78:81], v[82:85], a[56:59]
	v_mfma_f32_16x16x32_f16 a[68:71], v[78:81], v[86:89], a[68:71]
	s_waitcnt lgkmcnt(8)
	v_mfma_f32_16x16x32_f16 a[0:3], v[42:45], v[14:17], a[0:3]
	ds_read_b128 v[82:85], v157
	v_mfma_f32_16x16x32_f16 a[4:7], v[42:45], v[18:21], a[4:7]
	ds_read_b128 v[86:89], v159
	s_waitcnt lgkmcnt(9)
	v_mfma_f32_16x16x32_f16 a[12:15], v[38:41], v[14:17], a[12:15]
	ds_read_b128 v[70:73], v165 offset:9216
	v_mfma_f32_16x16x32_f16 a[16:19], v[38:41], v[18:21], a[16:19]
	ds_read_b128 v[66:69], v165 offset:10240
	s_waitcnt lgkmcnt(10)
	v_mfma_f32_16x16x32_f16 a[28:31], v[34:37], v[14:17], a[28:31]
	ds_read_b128 v[58:61], v165 offset:11264
	v_mfma_f32_16x16x32_f16 a[60:63], v[34:37], v[18:21], a[60:63]
	ds_read_b128 v[54:57], v165 offset:12288
	s_waitcnt lgkmcnt(11)
	v_mfma_f32_16x16x32_f16 a[8:11], v[30:33], v[14:17], a[8:11]
	ds_read_b128 v[46:49], v165 offset:13312
	v_mfma_f32_16x16x32_f16 a[20:23], v[30:33], v[18:21], a[20:23]
	ds_read_b128 v[50:53], v165 offset:14336
	s_waitcnt lgkmcnt(12)
	v_mfma_f32_16x16x32_f16 a[24:27], v[26:29], v[14:17], a[24:27]
	ds_read_b128 v[62:65], v165 offset:15360
	v_mfma_f32_16x16x32_f16 a[36:39], v[26:29], v[18:21], a[36:39]
	ds_read_b128 v[74:77], v165 offset:16384
	s_waitcnt lgkmcnt(13)
	v_mfma_f32_16x16x32_f16 a[44:47], v[22:25], v[14:17], a[44:47]
	ds_read_b128 v[78:81], v165 offset:17408
	v_mfma_f32_16x16x32_f16 a[64:67], v[22:25], v[18:21], a[64:67]
	s_waitcnt lgkmcnt(13)
	v_mfma_f32_16x16x32_f16 a[32:35], v[10:13], v[14:17], a[32:35]
	v_mfma_f32_16x16x32_f16 a[40:43], v[10:13], v[18:21], a[40:43]
	s_waitcnt lgkmcnt(12)
	v_mfma_f32_16x16x32_f16 a[48:51], v[6:9], v[14:17], a[48:51]
	v_mfma_f32_16x16x32_f16 a[52:55], v[6:9], v[18:21], a[52:55]
	s_waitcnt lgkmcnt(11)
	v_mfma_f32_16x16x32_f16 a[56:59], v[2:5], v[14:17], a[56:59]
	v_mfma_f32_16x16x32_f16 a[68:71], v[2:5], v[18:21], a[68:71]
	s_waitcnt vmcnt(6) lgkmcnt(0)
	s_barrier
	s_add_u32 s52, s50, 0x24000
	s_addc_u32 s53, s51, 0
	s_add_i32 m0, s42, 0xc600
	s_nop 0
	global_load_lds_dwordx4 v137, s[52:53]
	s_add_i32 m0, s43, 0xc600
	s_nop 0
	global_load_lds_dwordx4 v138, s[52:53]
	s_cmp_lt_u32 s42, 0x800
	s_cbranch_scc0 .Lk4_st6_8
	s_add_i32 m0, s44, 0xc600
	s_nop 0
	global_load_lds_dwordx4 v139, s[52:53]

.LBB3_32:
	s_barrier
	s_add_u32 s52, s10, 0x1000000
	s_addc_u32 s53, s11, 0
	v_add_u32_e32 v61, 0xe000, v118
	v_lshlrev_b32_e32 v62, 2, v94
	s_nop 0
	v_readfirstlane_b32 s44, v61
	s_mov_b32 m0, s44
	s_nop 0
	global_load_lds_dwordx4 v62, s[52:53] nt
	v_add_u32_e32 v61, 0xe000, v90
	v_lshlrev_b32_e32 v62, 2, v96
	s_nop 0
	v_readfirstlane_b32 s44, v61
	s_mov_b32 m0, s44
	s_nop 0
	global_load_lds_dwordx4 v62, s[52:53] nt
	v_add_u32_e32 v61, 0xe000, v91
	v_lshlrev_b32_e32 v62, 2, v98
	s_nop 0
	v_readfirstlane_b32 s44, v61
	s_mov_b32 m0, s44
	s_nop 0
	global_load_lds_dwordx4 v62, s[52:53] nt
	v_add_u32_e32 v61, 0xe000, v119
	v_lshlrev_b32_e32 v62, 2, v100
	s_nop 0
	v_readfirstlane_b32 s44, v61
	s_mov_b32 m0, s44
	s_nop 0
	global_load_lds_dwordx4 v62, s[52:53] nt
	v_mbcnt_lo_u32_b32 v63, -1, 0
	v_mbcnt_hi_u32_b32 v63, -1, v63
	v_lshlrev_b32_e32 v63, 4, v63
	v_add_u32_e32 v64, v91, v63
	v_add_u32_e32 v65, v119, v63
	v_add_u32_e32 v66, v118, v63
	v_add_u32_e32 v67, v90, v63
	ds_write_b128 v64, v[128:131]
	ds_write_b128 v65, v[132:135]
	ds_write_b128 v66, v[172:175] offset:28672
	ds_write_b128 v67, v[176:179] offset:28672
	ds_write_b128 v64, v[140:143] offset:28672
	ds_write_b128 v65, v[144:147] offset:28672
	v_lshl_add_u32 v0, v120, 5, s22
	v_or_b32_e32 v1, s23, v121
	s_movk_i32 s0, 0x7f
	v_lshl_or_b32 v7, v93, 1, v0
	s_movk_i32 s1, 0x7e
	s_nop 15
	s_nop 15
	v_cmp_eq_u32_e64 s[4:5], s1, v7
	s_nop 7
	v_cmp_gt_u32_e32 vcc, s0, v1
	v_accvgpr_read_b32 v5, a14
	v_cmp_eq_u32_e64 s[0:1], 0, v1
	v_or_b32_e32 v4, v93, v7
	v_cmp_eq_u32_e64 s[2:3], 0, v4
	v_cndmask_b32_e64 v14, v5, 0, s[0:1]
	v_accvgpr_read_b32 v5, a13
	v_cndmask_b32_e64 v22, v5, 0, s[0:1]
	v_accvgpr_read_b32 v5, a12
	v_cndmask_b32_e64 v116, v5, 0, s[0:1]
	v_accvgpr_read_b32 v5, a49
	v_cndmask_b32_e32 v16, 0, v5, vcc
	v_accvgpr_read_b32 v5, a48
	v_cndmask_b32_e32 v28, 0, v5, vcc
	v_accvgpr_read_b32 v5, a30
	v_cndmask_b32_e64 v10, v5, 0, s[0:1]
	v_accvgpr_read_b32 v5, a29
	v_cndmask_b32_e64 v24, v5, 0, s[0:1]
	v_accvgpr_read_b32 v5, a28
	v_cndmask_b32_e64 v42, v5, 0, s[0:1]
	v_accvgpr_read_b32 v5, a57
	v_cndmask_b32_e32 v20, 0, v5, vcc
	v_accvgpr_read_b32 v5, a56
	v_cndmask_b32_e32 v38, 0, v5, vcc
	v_accvgpr_read_b32 v5, a6
	v_cndmask_b32_e64 v15, v5, 0, s[0:1]
	v_accvgpr_read_b32 v5, a5
	v_cndmask_b32_e64 v23, v5, 0, s[0:1]
	v_accvgpr_read_b32 v5, a4
	v_cndmask_b32_e64 v117, v5, 0, s[0:1]
	v_accvgpr_read_b32 v5, a41
	v_cndmask_b32_e32 v17, 0, v5, vcc
	v_accvgpr_read_b32 v5, a40
	v_cndmask_b32_e32 v29, 0, v5, vcc
	v_accvgpr_read_b32 v5, a17
	v_cndmask_b32_e64 v37, v5, 0, s[0:1]
	v_accvgpr_read_b32 v5, a16
	v_cndmask_b32_e64 v47, v5, 0, s[0:1]
	v_accvgpr_read_b32 v5, a52
	v_cndmask_b32_e32 v45, 0, v5, vcc
	v_accvgpr_read_b32 v5, a68
	v_cndmask_b32_e32 v12, 0, v5, vcc
	v_accvgpr_read_b32 v5, a0
	s_or_b64 s[8:9], s[2:3], s[0:1]
	v_cmp_eq_u32_e64 s[6:7], 15, v93
	v_accvgpr_read_b32 v11, a8
	v_cndmask_b32_e64 v112, v5, 0, s[8:9]
	v_accvgpr_read_b32 v4, a67
	v_mov_b32_e32 v5, 0x90
	s_and_b64 s[4:5], s[6:7], s[4:5]
	v_mov_b64_e32 v[40:41], v[16:17]
	v_cndmask_b32_e64 v16, v11, 0, s[2:3]
	v_cndmask_b32_e64 v11, 12, v5, s[6:7]
	v_cndmask_b32_e64 v61, v4, 0, s[4:5]
	v_accvgpr_read_b32 v4, a61
	s_or_b64 s[6:7], s[4:5], s[0:1]
	v_cndmask_b32_e64 v87, v4, 0, s[6:7]
	v_accvgpr_read_b32 v4, a60
	v_cndmask_b32_e64 v86, v4, 0, s[6:7]
	v_accvgpr_read_b32 v4, a65
	v_cndmask_b32_e64 v5, v4, 0, s[4:5]
	v_accvgpr_read_b32 v4, a64
	v_cndmask_b32_e64 v4, v4, 0, s[4:5]
	s_lshl_b32 s14, s18, 2
	v_mov_b64_e32 v[32:33], v[4:5]
	v_lshl_or_b32 v4, v122, 18, s14
	v_mov_b32_e32 v5, 0
	v_mov_b64_e32 v[62:63], v[14:15]
	v_lshl_add_u64 v[14:15], s[12:13], 0, v[4:5]
	v_lshlrev_b32_e32 v4, 7, v1
	v_lshl_add_u64 v[14:15], v[4:5], 2, v[14:15]
	v_lshlrev_b32_e32 v4, 2, v7
	v_mul_u32_u24_e32 v1, 24, v122
	v_lshl_add_u64 v[54:55], v[14:15], 0, v[4:5]
	v_mbcnt_lo_u32_b32 v138, -1, 0
	v_mbcnt_hi_u32_b32 v138, -1, v138
	v_and_b32_e32 v138, 1, v138
	v_mul_u32_u24_e32 v138, 0xfff8, v138
	v_add_u32_e32 v138, 0xffff0000, v138
	v_mov_b32_e32 v139, -1
	v_lshl_add_u64 v[134:135], v[54:55], 0, v[138:139]
	s_mov_b32 s28, 0x55555555
	s_mov_b32 s29, 0x55555555
	s_mov_b32 s30, 0xaaaaaaaa
	s_mov_b32 s31, 0xaaaaaaaa
	v_or_b32_e32 v1, v1, v121
	v_lshlrev_b32_e32 v4, 7, v120
	s_movk_i32 s12, 0x120
	v_mad_u32_u24 v1, v1, s12, v4
	s_add_u32 s12, s10, 0x800000
	v_accvgpr_read_b32 v7, a72
	v_mov_b64_e32 v[80:81], v[28:29]
	s_addc_u32 s13, s11, 0
	v_lshlrev_b64 v[28:29], 2, v[94:95]
	v_readfirstlane_b32 s14, v7
	v_add_u32_e32 v7, 0, v90
	v_lshl_add_u64 v[4:5], s[12:13], 0, v[28:29]
	s_mov_b32 m0, s14
	v_lshlrev_b64 v[30:31], 2, v[96:97]
	v_readfirstlane_b32 s14, v7
	v_mov_b32_e32 v14, v7
	v_add_u32_e32 v7, 0, v91
	s_waitcnt lgkmcnt(0)
	v_lshlrev_b64 v[56:57], 2, v[98:99]
	v_mov_b32_e32 v19, v7
	v_lshlrev_b64 v[58:59], 2, v[100:101]
	v_add_u32_e32 v7, 0, v119
	v_accvgpr_read_b32 v25, a72
	v_mov_b32_e32 v21, v7
	v_lshl_add_u32 v15, v93, 3, v1
	v_add_u32_e32 v1, v1, v11
	s_waitcnt vmcnt(16)
	v_accvgpr_write_b32 a12, v14
	v_mov_b64_e32 v[124:125], v[56:57]
	v_accvgpr_write_b32 a13, v19
	v_mov_b64_e32 v[126:127], v[58:59]
	v_accvgpr_write_b32 a16, v21
	s_waitcnt lgkmcnt(0)
	s_barrier
	v_add_u32_e32 v14, 0x16010, v15
	v_mov_b32_e32 v122, v15
	v_add_u32_e32 v15, 0x16000, v1
	ds_read_b64 v[64:65], v14
	ds_read_b64 v[66:67], v14 offset:288
	ds_read_b64 v[68:69], v14 offset:576
	ds_read_b64 v[76:77], v14 offset:1728
	ds_read_b64 v[78:79], v14 offset:2016
	ds_read_b64 v[4:5], v14 offset:2304
	ds_read_b64 v[84:85], v14 offset:3456
	ds_read_b64 v[74:75], v14 offset:3744
	ds_read_b64 v[88:89], v14 offset:4032
	ds_read_b64 v[100:101], v14 offset:5184
	ds_read_b64 v[106:107], v14 offset:5472
	ds_read_b64 v[120:121], v14 offset:5760
	ds_read_b32 v43, v15
	ds_read_b32 v19, v15 offset:288
	ds_read_b32 v39, v15 offset:576
	ds_read_b32 v25, v15 offset:1728
	ds_read_b32 v7, v15 offset:2016
	ds_read_b32 v21, v15 offset:2304
	ds_read_b32 v11, v15 offset:3456
	ds_read_b32 v35, v15 offset:3744
	ds_read_b32 v59, v15 offset:4032
	ds_read_b32 v57, v15 offset:5184
	ds_read_b32 v51, v15 offset:5472
	ds_read_b32 v49, v15 offset:5760
	s_waitcnt lgkmcnt(0)
	v_accvgpr_read_b32 v8, a26
	v_mov_b32_e32 v46, v43
	v_mov_b32_e32 v113, v65
	v_mov_b32_e32 v26, v19
	v_mov_b32_dpp v46, v65 row_shr:1 row_mask:0xf bank_mask:0xf
	v_pk_mul_f32 v[70:71], v[112:113], v[46:47]
	v_accvgpr_read_b32 v9, a22
	v_accvgpr_read_b32 v27, a36
	v_mov_b32_dpp v43, v64 row_shl:1 row_mask:0xf bank_mask:0xf
	v_mov_b32_dpp v26, v67 row_shr:1 row_mask:0xf bank_mask:0xf
	v_pk_fma_f32 v[70:71], v[64:65], v[116:117], v[70:71] op_sel_hi:[0,1,1]
	v_pk_mov_b32 v[64:65], v[64:65], v[86:87] op_sel:[1,0]
	v_mov_b32_e32 v17, v67
	v_mov_b64_e32 v[102:103], v[8:9]
	v_accvgpr_read_b32 v8, a25
	v_accvgpr_read_b32 v114, a24
	v_accvgpr_read_b32 v9, a21
	v_accvgpr_read_b32 v115, a20
	v_accvgpr_read_b32 v2, a32
	v_mov_b64_e32 v[82:83], v[30:31]
	v_pk_fma_f32 v[70:71], v[64:65], v[42:43], v[70:71]
	v_pk_mul_f32 v[64:65], v[16:17], v[26:27]
	v_mov_b64_e32 v[30:31], v[32:33]
	v_accvgpr_read_b32 v18, a44
	v_mov_b64_e32 v[104:105], v[8:9]
	v_cndmask_b32_e32 v9, 0, v2, vcc
	v_accvgpr_write_b32 a4, v14
	v_mov_b32_dpp v19, v66 row_shl:1 row_mask:0xf bank_mask:0xf
	v_pk_fma_f32 v[64:65], v[66:67], v[114:115], v[64:65] op_sel_hi:[0,1,1]
	v_pk_mov_b32 v[66:67], v[66:67], v[30:31] op_sel:[1,0]
	v_accvgpr_read_b32 v14, a69
	v_mov_b32_e32 v44, v39
	v_mov_b32_e32 v60, v1
	v_pk_fma_f32 v[66:67], v[66:67], v[18:19], v[64:65]
	v_cndmask_b32_e32 v14, 0, v14, vcc
	v_cndmask_b32_e64 v0, v9, 0, s[2:3]
	v_mov_b32_dpp v44, v69 row_shr:1 row_mask:0xf bank_mask:0xf
	v_pk_add_f32 v[70:71], v[70:71], 0 op_sel_hi:[1,0]
	v_mov_b32_e32 v1, v69
	v_accvgpr_write_b32 a0, v15
	v_cndmask_b32_e64 v15, v14, 0, s[4:5]
	v_cndmask_b32_e64 v14, v12, 0, s[4:5]
	v_pk_add_f32 v[66:67], v[70:71], v[66:67]
	v_pk_mul_f32 v[70:71], v[0:1], v[44:45]
	v_mov_b32_dpp v39, v68 row_shl:1 row_mask:0xf bank_mask:0xf
	v_pk_fma_f32 v[70:71], v[68:69], v[80:81], v[70:71] op_sel_hi:[0,1,1]
	v_pk_mov_b32 v[68:69], v[68:69], v[14:15] op_sel:[1,0]
	v_accvgpr_read_b32 v9, a1
	v_pk_fma_f32 v[68:69], v[68:69], v[38:39], v[70:71]
	v_mov_b32_e32 v36, v25
	v_cndmask_b32_e64 v64, v9, 0, s[8:9]
	v_pk_add_f32 v[66:67], v[66:67], v[68:69]
	v_mov_b32_dpp v36, v77 row_shr:1 row_mask:0xf bank_mask:0xf
	v_mov_b32_e32 v65, v77
	v_mov_b64_e32 v[108:109], v[22:23]
	v_accvgpr_read_b32 v9, a9
	v_mov_b32_e32 v128, v66
	v_mov_b32_e32 v129, v67
	v_mov_b32_e32 v12, v7
	v_pk_mul_f32 v[66:67], v[64:65], v[36:37]
	v_accvgpr_read_b32 v13, a37
	v_mov_b64_e32 v[72:73], v[28:29]
	v_cndmask_b32_e64 v28, v9, 0, s[2:3]
	v_mov_b32_dpp v25, v76 row_shl:1 row_mask:0xf bank_mask:0xf
	v_mov_b32_dpp v12, v79 row_shr:1 row_mask:0xf bank_mask:0xf
	v_pk_fma_f32 v[66:67], v[76:77], v[108:109], v[66:67] op_sel_hi:[0,1,1]
	v_mov_b32_e32 v76, v77
	v_mov_b32_e32 v77, v87
	v_mov_b32_e32 v29, v79
	v_pk_fma_f32 v[66:67], v[76:77], v[24:25], v[66:67]
	v_pk_mul_f32 v[76:77], v[28:29], v[12:13]
	v_accvgpr_read_b32 v6, a45
	v_accvgpr_read_b32 v2, a33
	v_mov_b32_dpp v7, v78 row_shl:1 row_mask:0xf bank_mask:0xf
	v_pk_fma_f32 v[76:77], v[78:79], v[104:105], v[76:77] op_sel_hi:[0,1,1]
	v_mov_b32_e32 v78, v79
	v_mov_b32_e32 v79, v31
	v_cndmask_b32_e32 v2, 0, v2, vcc
	v_accvgpr_read_b32 v50, a53
	v_pk_fma_f32 v[76:77], v[78:79], v[6:7], v[76:77]
	v_mov_b32_e32 v78, v21
	v_accvgpr_write_b32 a44, v80
	v_cndmask_b32_e32 v79, 0, v50, vcc
	v_cndmask_b32_e64 v52, v2, 0, s[2:3]
	v_mov_b32_dpp v78, v5 row_shr:1 row_mask:0xf bank_mask:0xf
	v_pk_add_f32 v[66:67], v[66:67], 0 op_sel_hi:[1,0]
	v_mov_b32_e32 v53, v5
	v_accvgpr_write_b32 a45, v81
	v_accvgpr_write_b32 a21, v15
	v_pk_add_f32 v[80:81], v[66:67], v[76:77]
	v_pk_mul_f32 v[66:67], v[52:53], v[78:79]
	v_accvgpr_write_b32 a24, v40
	v_accvgpr_read_b32 v2, a2
	v_mov_b32_dpp v21, v4 row_shl:1 row_mask:0xf bank_mask:0xf
	v_pk_fma_f32 v[66:67], v[4:5], v[40:41], v[66:67] op_sel_hi:[0,1,1]
	v_accvgpr_write_b32 a25, v41
	v_mov_b32_e32 v4, v5
	v_accvgpr_read_b32 v5, a21
	v_cndmask_b32_e64 v40, v2, 0, s[8:9]
	v_accvgpr_read_b32 v2, a62
	v_accvgpr_read_b32 v8, a18
	v_accvgpr_read_b32 v48, a63
	v_accvgpr_write_b32 a20, v14
	v_accvgpr_write_b32 a41, v23
	v_pk_fma_f32 v[4:5], v[4:5], v[20:21], v[66:67]
	s_mov_b64 s[12:13], 0x10000
	v_cndmask_b32_e64 v14, v2, 0, s[6:7]
	v_mov_b32_e32 v76, v11
	v_accvgpr_read_b32 v2, a10
	v_accvgpr_write_b32 a40, v22
	v_cndmask_b32_e64 v15, v48, 0, s[6:7]
	v_cndmask_b32_e64 v77, v8, 0, s[0:1]
	v_pk_add_f32 v[4:5], v[80:81], v[4:5]
	v_lshl_add_u64 v[136:137], v[134:135], 0, s[12:13]
	v_mov_b32_dpp v76, v85 row_shr:1 row_mask:0xf bank_mask:0xf
	v_mov_b32_e32 v41, v85
	v_cndmask_b32_e64 v22, v2, 0, s[2:3]
	v_mov_b32_e32 v2, v35
	v_accvgpr_read_b32 v1, a50
	v_accvgpr_read_b32 v3, a38
	s_mov_b64 s[32:33], vcc
	s_nop 1
	s_mov_b64 vcc, s[28:29]
	s_nop 0
	v_cndmask_b32_dpp v130, v4, v128, vcc quad_perm:[1,0,3,2] row_mask:0xf bank_mask:0xf
	v_cndmask_b32_dpp v131, v5, v129, vcc quad_perm:[1,0,3,2] row_mask:0xf bank_mask:0xf
	s_mov_b64 vcc, s[30:31]
	s_nop 0
	v_cndmask_b32_dpp v132, v128, v4, vcc quad_perm:[1,0,3,2] row_mask:0xf bank_mask:0xf
	v_cndmask_b32_dpp v133, v129, v5, vcc quad_perm:[1,0,3,2] row_mask:0xf bank_mask:0xf
	global_store_dwordx4 v[136:137], v[130:133], off sc0 sc1 nt
	s_nop 1
	s_mov_b64 vcc, s[32:33]
	v_mov_b64_e32 v[8:9], v[14:15]
	v_pk_mul_f32 v[4:5], v[40:41], v[76:77]
	v_mov_b64_e32 v[66:67], v[62:63]
	v_mov_b32_dpp v2, v75 row_shr:1 row_mask:0xf bank_mask:0xf
	v_mov_b32_e32 v23, v75
	v_cndmask_b32_e32 v62, 0, v1, vcc
	v_accvgpr_read_b32 v1, a42
	v_mov_b32_dpp v11, v84 row_shl:1 row_mask:0xf bank_mask:0xf
	v_pk_fma_f32 v[4:5], v[84:85], v[66:67], v[4:5] op_sel_hi:[0,1,1]
	v_pk_mov_b32 v[80:81], v[84:85], v[8:9] op_sel:[1,0]
	v_pk_mul_f32 v[84:85], v[22:23], v[2:3]
	v_accvgpr_read_b32 v2, a58
	v_cndmask_b32_e32 v63, 0, v1, vcc
	v_accvgpr_read_b32 v1, a70
	v_pk_fma_f32 v[80:81], v[80:81], v[10:11], v[4:5]
	v_accvgpr_read_b32 v4, a66
	v_cndmask_b32_e32 v58, 0, v2, vcc
	v_cndmask_b32_e32 v1, 0, v1, vcc
	v_accvgpr_read_b32 v2, a71
	v_cndmask_b32_e64 v8, v4, 0, s[4:5]
	v_cndmask_b32_e32 v2, 0, v2, vcc
	v_cndmask_b32_e64 v4, v1, 0, s[4:5]
	v_accvgpr_read_b32 v1, a34
	v_mov_b32_e32 v9, v61
	v_cndmask_b32_e64 v5, v2, 0, s[4:5]
	v_cndmask_b32_e32 v1, 0, v1, vcc
	v_accvgpr_read_b32 v2, a54
	v_mov_b32_e32 v92, v59
	v_accvgpr_read_b32 v34, a46
	v_mov_b32_dpp v35, v74 row_shl:1 row_mask:0xf bank_mask:0xf
	v_pk_fma_f32 v[84:85], v[74:75], v[102:103], v[84:85] op_sel_hi:[0,1,1]
	v_pk_mov_b32 v[74:75], v[74:75], v[8:9] op_sel:[1,0]
	v_cndmask_b32_e32 v93, 0, v2, vcc
	v_mov_b32_dpp v92, v89 row_shr:1 row_mask:0xf bank_mask:0xf
	v_cndmask_b32_e64 v96, v1, 0, s[2:3]
	v_mov_b32_e32 v97, v89
	v_accvgpr_read_b32 v1, a31
	v_pk_fma_f32 v[74:75], v[74:75], v[34:35], v[84:85]
	v_pk_mul_f32 v[84:85], v[96:97], v[92:93]
	v_accvgpr_write_b32 a8, v62
	v_cndmask_b32_e64 v56, v1, 0, s[0:1]
	v_accvgpr_read_b32 v1, a15
	v_pk_fma_f32 v[84:85], v[88:89], v[62:63], v[84:85] op_sel_hi:[0,1,1]
	v_accvgpr_write_b32 a9, v63
	v_cndmask_b32_e64 v62, v1, 0, s[0:1]
	v_accvgpr_read_b32 v1, a7
	v_cndmask_b32_e64 v63, v1, 0, s[0:1]
	v_accvgpr_read_b32 v1, a19
	v_pk_add_f32 v[80:81], v[80:81], 0 op_sel_hi:[1,0]
	v_mov_b32_dpp v59, v88 row_shl:1 row_mask:0xf bank_mask:0xf
	v_pk_mov_b32 v[88:89], v[88:89], v[4:5] op_sel:[1,0]
	v_cndmask_b32_e64 v95, v1, 0, s[0:1]
	v_accvgpr_read_b32 v1, a3
	v_accvgpr_write_b32 a36, v104
	v_pk_add_f32 v[80:81], v[80:81], v[74:75]
	v_pk_fma_f32 v[84:85], v[88:89], v[58:59], v[84:85]
	v_mov_b32_e32 v94, v57
	v_cndmask_b32_e64 v98, v1, 0, s[8:9]
	v_accvgpr_read_b32 v1, a11
	v_accvgpr_write_b32 a37, v105
	v_accvgpr_write_b32 a32, v102
	v_pk_add_f32 v[80:81], v[80:81], v[84:85]
	s_mov_b64 s[4:5], 0x20000
	v_mov_b32_dpp v94, v101 row_shr:1 row_mask:0xf bank_mask:0xf
	v_mov_b32_e32 v99, v101
	v_cndmask_b32_e64 v104, v1, 0, s[2:3]
	v_accvgpr_read_b32 v1, a59
	v_accvgpr_write_b32 a29, v15
	v_accvgpr_write_b32 a33, v103
	v_accvgpr_write_b32 a49, v5
	v_lshl_add_u64 v[84:85], v[54:55], 0, s[4:5]
	v_mov_b32_e32 v128, v80
	v_mov_b32_e32 v129, v81
	v_pk_mul_f32 v[80:81], v[98:99], v[94:95]
	v_mov_b32_e32 v102, v51
	v_cndmask_b32_e32 v48, 0, v1, vcc
	v_accvgpr_read_b32 v1, a51
	v_accvgpr_write_b32 a48, v4
	v_mov_b32_dpp v57, v100 row_shl:1 row_mask:0xf bank_mask:0xf
	v_pk_fma_f32 v[80:81], v[100:101], v[62:63], v[80:81] op_sel_hi:[0,1,1]
	v_mov_b32_e32 v84, v101
	v_accvgpr_read_b32 v85, a29
	v_accvgpr_read_b32 v103, a39
	v_mov_b32_dpp v102, v107 row_shr:1 row_mask:0xf bank_mask:0xf
	v_mov_b32_e32 v105, v107
	v_cndmask_b32_e32 v4, 0, v1, vcc
	v_accvgpr_read_b32 v1, a43
	v_pk_fma_f32 v[80:81], v[84:85], v[56:57], v[80:81]
	v_accvgpr_read_b32 v30, a27
	v_accvgpr_read_b32 v31, a23
	v_pk_mul_f32 v[84:85], v[104:105], v[102:103]
	v_cndmask_b32_e32 v5, 0, v1, vcc
	v_accvgpr_read_b32 v1, a35
	v_accvgpr_read_b32 v50, a47
	v_mov_b32_dpp v51, v106 row_shl:1 row_mask:0xf bank_mask:0xf
	v_pk_fma_f32 v[84:85], v[106:107], v[30:31], v[84:85] op_sel_hi:[0,1,1]
	v_mov_b32_e32 v106, v107
	v_mov_b32_e32 v107, v9
	v_cndmask_b32_e32 v1, 0, v1, vcc
	v_accvgpr_read_b32 v2, a55
	v_mov_b32_e32 v108, v49
	v_pk_fma_f32 v[84:85], v[106:107], v[50:51], v[84:85]
	v_pk_add_f32 v[80:81], v[80:81], 0 op_sel_hi:[1,0]
	v_cndmask_b32_e32 v109, 0, v2, vcc
	v_mov_b32_dpp v108, v121 row_shr:1 row_mask:0xf bank_mask:0xf
	v_cndmask_b32_e64 v110, v1, 0, s[2:3]
	v_mov_b32_e32 v111, v121
	v_pk_add_f32 v[80:81], v[80:81], v[84:85]
	v_pk_mul_f32 v[84:85], v[110:111], v[108:109]
	v_mov_b32_dpp v49, v120 row_shl:1 row_mask:0xf bank_mask:0xf
	v_pk_fma_f32 v[84:85], v[120:121], v[4:5], v[84:85] op_sel_hi:[0,1,1]
	v_mov_b32_e32 v120, v121
	v_accvgpr_read_b32 v121, a49
	v_pk_fma_f32 v[84:85], v[120:121], v[48:49], v[84:85]
	s_mov_b64 s[0:1], 0x30000
	v_pk_add_f32 v[80:81], v[80:81], v[84:85]
	v_lshl_add_u64 v[136:137], v[134:135], 0, s[0:1]
	v_add_u32_e32 v1, s17, v118
	s_add_u32 s0, s10, 0x1400000
	s_mov_b64 s[32:33], vcc
	s_nop 1
	s_mov_b64 vcc, s[28:29]
	s_nop 0
	v_cndmask_b32_dpp v130, v80, v128, vcc quad_perm:[1,0,3,2] row_mask:0xf bank_mask:0xf
	v_cndmask_b32_dpp v131, v81, v129, vcc quad_perm:[1,0,3,2] row_mask:0xf bank_mask:0xf
	s_mov_b64 vcc, s[30:31]
	s_nop 0
	v_cndmask_b32_dpp v132, v128, v80, vcc quad_perm:[1,0,3,2] row_mask:0xf bank_mask:0xf
	v_cndmask_b32_dpp v133, v129, v81, vcc quad_perm:[1,0,3,2] row_mask:0xf bank_mask:0xf
	global_store_dwordx4 v[136:137], v[130:133], off sc0 sc1 nt
	s_nop 1
	s_mov_b64 vcc, s[32:33]
	v_readfirstlane_b32 s2, v1
	s_addc_u32 s1, s11, 0
	v_add_u32_e32 v1, s17, v90
	s_waitcnt vmcnt(6)
	v_lshl_add_u64 v[80:81], s[0:1], 0, v[72:73]
	s_mov_b32 m0, s2
	v_readfirstlane_b32 s2, v1
	v_mov_b64_e32 v[74:75], v[82:83]
	v_add_u32_e32 v1, s17, v91
	s_waitcnt lgkmcnt(0)
	s_barrier
	global_load_lds_dwordx4 v[80:81], off nt
	v_lshl_add_u64 v[80:81], s[0:1], 0, v[74:75]
	s_mov_b32 m0, s2
	v_readfirstlane_b32 s2, v1
	v_add_u32_e32 v1, s17, v119
	global_load_lds_dwordx4 v[80:81], off nt
	v_lshl_add_u64 v[80:81], s[0:1], 0, v[124:125]
	s_mov_b32 m0, s2
	v_readfirstlane_b32 s2, v1
	global_load_lds_dwordx4 v[80:81], off nt
	v_lshl_add_u64 v[80:81], s[0:1], 0, v[126:127]
	s_mov_b32 m0, s2
	v_accvgpr_write_b32 a53, v33
	v_accvgpr_write_b32 a2, v62
	v_accvgpr_write_b32 a7, v5
	v_accvgpr_write_b32 a22, v124
	v_accvgpr_write_b32 a30, v126
	global_load_lds_dwordx4 v[80:81], off nt
	v_accvgpr_write_b32 a52, v32
	v_accvgpr_write_b32 a3, v63
	v_accvgpr_write_b32 a6, v4
	v_mov_b64_e32 v[32:33], v[72:73]
	v_accvgpr_write_b32 a23, v125
	v_accvgpr_write_b32 a31, v127
	v_add_u32_e32 v2, 0x1d010, v122
	v_accvgpr_write_b32 a10, v122
	v_add_u32_e32 v5, 0x1d000, v60
	v_mov_b32_e32 v4, v60
	ds_read_b64 v[62:63], v2
	ds_read_b64 v[60:61], v2 offset:288
	ds_read_b64 v[72:73], v2 offset:576
	ds_read_b64 v[70:71], v2 offset:1728
	ds_read_b64 v[68:69], v2 offset:2016
	ds_read_b64 v[82:83], v2 offset:2304
	ds_read_b64 v[80:81], v2 offset:3456
	ds_read_b64 v[84:85], v2 offset:3744
	ds_read_b64 v[126:127], v2 offset:4032
	ds_read_b64 v[124:125], v2 offset:5184
	ds_read_b64 v[122:123], v2 offset:5472
	ds_read_b64 v[120:121], v2 offset:5760
	ds_read_b32 v43, v5
	ds_read_b32 v19, v5 offset:288
	ds_read_b32 v39, v5 offset:576
	ds_read_b32 v25, v5 offset:1728
	ds_read_b32 v7, v5 offset:2016
	ds_read_b32 v21, v5 offset:2304
	ds_read_b32 v11, v5 offset:3456
	ds_read_b32 v35, v5 offset:3744
	ds_read_b32 v59, v5 offset:4032
	ds_read_b32 v57, v5 offset:5184
	ds_read_b32 v51, v5 offset:5472
	ds_read_b32 v49, v5 offset:5760
	s_waitcnt lgkmcnt(0)
	v_mov_b64_e32 v[100:101], v[86:87]
	v_mov_b32_e32 v46, v43
	v_mov_b32_e32 v113, v63
	v_mov_b32_e32 v26, v19
	v_mov_b32_dpp v46, v63 row_shr:1 row_mask:0xf bank_mask:0xf
	v_pk_mul_f32 v[88:89], v[112:113], v[46:47]
	v_mov_b32_dpp v43, v62 row_shl:1 row_mask:0xf bank_mask:0xf
	v_pk_fma_f32 v[88:89], v[62:63], v[116:117], v[88:89] op_sel_hi:[0,1,1]
	v_pk_mov_b32 v[62:63], v[62:63], v[100:101] op_sel:[1,0]
	v_mov_b32_dpp v26, v61 row_shr:1 row_mask:0xf bank_mask:0xf
	v_mov_b32_e32 v17, v61
	v_pk_fma_f32 v[62:63], v[62:63], v[42:43], v[88:89]
	v_pk_mul_f32 v[88:89], v[16:17], v[26:27]
	v_accvgpr_write_b32 a34, v16
	v_accvgpr_read_b32 v16, a52
	v_accvgpr_read_b32 v17, a53
	v_mov_b32_dpp v19, v60 row_shl:1 row_mask:0xf bank_mask:0xf
	v_pk_fma_f32 v[88:89], v[60:61], v[114:115], v[88:89] op_sel_hi:[0,1,1]
	v_pk_mov_b32 v[60:61], v[60:61], v[16:17] op_sel:[1,0]
	v_mov_b32_e32 v44, v39
	v_accvgpr_write_b32 a28, v14
	v_pk_fma_f32 v[60:61], v[60:61], v[18:19], v[88:89]
	v_pk_add_f32 v[62:63], v[62:63], 0 op_sel_hi:[1,0]
	v_mov_b32_dpp v44, v73 row_shr:1 row_mask:0xf bank_mask:0xf
	v_mov_b32_e32 v1, v73
	v_accvgpr_read_b32 v14, a44
	v_accvgpr_read_b32 v89, a21
	v_pk_add_f32 v[60:61], v[62:63], v[60:61]
	v_pk_mul_f32 v[62:63], v[0:1], v[44:45]
	v_accvgpr_read_b32 v15, a45
	v_accvgpr_read_b32 v88, a20
	v_mov_b32_dpp v39, v72 row_shl:1 row_mask:0xf bank_mask:0xf
	v_pk_fma_f32 v[62:63], v[72:73], v[14:15], v[62:63] op_sel_hi:[0,1,1]
	v_pk_mov_b32 v[72:73], v[72:73], v[88:89] op_sel:[1,0]
	v_mov_b32_e32 v36, v25
	v_pk_fma_f32 v[62:63], v[72:73], v[38:39], v[62:63]
	s_mov_b64 s[0:1], 0x400000
	v_pk_add_f32 v[60:61], v[60:61], v[62:63]
	v_mov_b32_dpp v36, v71 row_shr:1 row_mask:0xf bank_mask:0xf
	v_mov_b32_e32 v65, v71
	v_accvgpr_read_b32 v87, a41
	v_lshl_add_u64 v[62:63], v[54:55], 0, s[0:1]
	v_mov_b32_e32 v128, v60
	v_mov_b32_e32 v129, v61
	v_pk_mul_f32 v[60:61], v[64:65], v[36:37]
	v_accvgpr_read_b32 v86, a40
	v_mov_b32_e32 v12, v7
	v_mov_b32_dpp v25, v70 row_shl:1 row_mask:0xf bank_mask:0xf
	v_pk_fma_f32 v[60:61], v[70:71], v[86:87], v[60:61] op_sel_hi:[0,1,1]
	v_mov_b32_e32 v62, v71
	v_mov_b32_e32 v63, v101
	v_mov_b32_dpp v12, v69 row_shr:1 row_mask:0xf bank_mask:0xf
	v_mov_b32_e32 v29, v69
	v_accvgpr_read_b32 v107, a37
	v_pk_fma_f32 v[60:61], v[62:63], v[24:25], v[60:61]
	v_pk_mul_f32 v[62:63], v[28:29], v[12:13]
	v_accvgpr_read_b32 v106, a36
	v_mov_b32_dpp v7, v68 row_shl:1 row_mask:0xf bank_mask:0xf
	v_pk_fma_f32 v[62:63], v[68:69], v[106:107], v[62:63] op_sel_hi:[0,1,1]
	v_mov_b32_e32 v68, v69
	v_mov_b32_e32 v69, v17
	v_mov_b32_e32 v78, v21
	v_pk_fma_f32 v[62:63], v[68:69], v[6:7], v[62:63]
	v_pk_add_f32 v[60:61], v[60:61], 0 op_sel_hi:[1,0]
	v_mov_b32_dpp v78, v83 row_shr:1 row_mask:0xf bank_mask:0xf
	v_mov_b32_e32 v53, v83
	v_accvgpr_read_b32 v14, a24
	v_pk_add_f32 v[60:61], v[60:61], v[62:63]
	v_pk_mul_f32 v[62:63], v[52:53], v[78:79]
	v_accvgpr_read_b32 v15, a25
	v_mov_b32_dpp v21, v82 row_shl:1 row_mask:0xf bank_mask:0xf
	v_pk_fma_f32 v[62:63], v[82:83], v[14:15], v[62:63] op_sel_hi:[0,1,1]
	v_mov_b32_e32 v68, v83
	v_mov_b32_e32 v69, v89
	v_pk_fma_f32 v[62:63], v[68:69], v[20:21], v[62:63]
	v_mov_b32_e32 v76, v11
	v_pk_add_f32 v[60:61], v[60:61], v[62:63]
	s_mov_b64 s[0:1], 0x410000
	v_mov_b32_dpp v76, v81 row_shr:1 row_mask:0xf bank_mask:0xf
	v_mov_b32_e32 v41, v81
	v_lshl_add_u64 v[136:137], v[134:135], 0, s[0:1]
	s_nop 1
	s_mov_b64 vcc, s[28:29]
	s_nop 0
	v_cndmask_b32_dpp v130, v60, v128, vcc quad_perm:[1,0,3,2] row_mask:0xf bank_mask:0xf
	v_cndmask_b32_dpp v131, v61, v129, vcc quad_perm:[1,0,3,2] row_mask:0xf bank_mask:0xf
	s_mov_b64 vcc, s[30:31]
	s_nop 0
	v_cndmask_b32_dpp v132, v128, v60, vcc quad_perm:[1,0,3,2] row_mask:0xf bank_mask:0xf
	v_cndmask_b32_dpp v133, v129, v61, vcc quad_perm:[1,0,3,2] row_mask:0xf bank_mask:0xf
	global_store_dwordx4 v[136:137], v[130:133], off sc0 sc1 nt
	s_nop 1
	v_pk_mul_f32 v[60:61], v[40:41], v[76:77]
	v_accvgpr_write_b32 a36, v66
	v_pk_fma_f32 v[60:61], v[80:81], v[66:67], v[60:61] op_sel_hi:[0,1,1]
	v_accvgpr_write_b32 a37, v67
	v_accvgpr_read_b32 v67, a29
	v_accvgpr_write_b32 a5, v2
	v_accvgpr_write_b32 a38, v100
	v_accvgpr_read_b32 v66, a28
	v_mov_b32_e32 v2, v35
	v_accvgpr_write_b32 a39, v101
	v_mov_b32_dpp v11, v80 row_shl:1 row_mask:0xf bank_mask:0xf
	v_pk_mov_b32 v[62:63], v[80:81], v[66:67] op_sel:[1,0]
	v_mov_b32_dpp v2, v85 row_shr:1 row_mask:0xf bank_mask:0xf
	v_mov_b32_e32 v23, v85
	v_accvgpr_read_b32 v101, a33
	v_pk_fma_f32 v[60:61], v[62:63], v[10:11], v[60:61]
	v_pk_mul_f32 v[62:63], v[22:23], v[2:3]
	v_accvgpr_read_b32 v100, a32
	v_mov_b32_dpp v35, v84 row_shl:1 row_mask:0xf bank_mask:0xf
	v_pk_fma_f32 v[62:63], v[84:85], v[100:101], v[62:63] op_sel_hi:[0,1,1]
	v_pk_mov_b32 v[68:69], v[84:85], v[8:9] op_sel:[1,0]
	v_mov_b32_e32 v92, v59
	v_pk_fma_f32 v[62:63], v[68:69], v[34:35], v[62:63]
	v_pk_add_f32 v[60:61], v[60:61], 0 op_sel_hi:[1,0]
	v_mov_b32_dpp v92, v127 row_shr:1 row_mask:0xf bank_mask:0xf
	v_mov_b32_e32 v97, v127
	v_accvgpr_read_b32 v17, a9
	v_accvgpr_read_b32 v71, a49
	v_pk_add_f32 v[60:61], v[60:61], v[62:63]
	v_pk_mul_f32 v[62:63], v[96:97], v[92:93]
	v_accvgpr_read_b32 v16, a8
	v_accvgpr_read_b32 v70, a48
	v_mov_b32_dpp v59, v126 row_shl:1 row_mask:0xf bank_mask:0xf
	v_pk_fma_f32 v[62:63], v[126:127], v[16:17], v[62:63] op_sel_hi:[0,1,1]
	v_pk_mov_b32 v[68:69], v[126:127], v[70:71] op_sel:[1,0]
	v_mov_b32_e32 v94, v57
	v_pk_fma_f32 v[62:63], v[68:69], v[58:59], v[62:63]
	v_accvgpr_write_b32 a20, v28
	v_pk_add_f32 v[60:61], v[60:61], v[62:63]
	s_mov_b64 s[0:1], 0x420000
	v_mov_b32_dpp v94, v125 row_shr:1 row_mask:0xf bank_mask:0xf
	v_mov_b32_e32 v99, v125
	v_accvgpr_read_b32 v29, a3
	v_lshl_add_u64 v[62:63], v[54:55], 0, s[0:1]
	v_mov_b32_e32 v128, v60
	v_mov_b32_e32 v129, v61
	v_pk_mul_f32 v[60:61], v[98:99], v[94:95]
	v_accvgpr_read_b32 v28, a2
	v_mov_b32_e32 v102, v51
	v_mov_b32_dpp v57, v124 row_shl:1 row_mask:0xf bank_mask:0xf
	v_pk_fma_f32 v[60:61], v[124:125], v[28:29], v[60:61] op_sel_hi:[0,1,1]
	v_mov_b32_e32 v62, v125
	v_mov_b32_e32 v63, v67
	v_mov_b32_dpp v102, v123 row_shr:1 row_mask:0xf bank_mask:0xf
	v_mov_b32_e32 v105, v123
	v_pk_fma_f32 v[60:61], v[62:63], v[56:57], v[60:61]
	v_pk_mul_f32 v[62:63], v[104:105], v[102:103]
	v_mov_b32_dpp v51, v122 row_shl:1 row_mask:0xf bank_mask:0xf
	v_pk_fma_f32 v[62:63], v[122:123], v[30:31], v[62:63] op_sel_hi:[0,1,1]
	v_accvgpr_write_b32 a28, v30
	v_mov_b32_e32 v68, v123
	v_mov_b32_e32 v69, v9
	v_mov_b32_e32 v108, v49
	v_accvgpr_write_b32 a29, v31
	v_pk_fma_f32 v[62:63], v[68:69], v[50:51], v[62:63]
	v_pk_add_f32 v[60:61], v[60:61], 0 op_sel_hi:[1,0]
	v_mov_b32_dpp v108, v121 row_shr:1 row_mask:0xf bank_mask:0xf
	v_mov_b32_e32 v111, v121
	v_accvgpr_read_b32 v31, a7
	v_pk_add_f32 v[60:61], v[60:61], v[62:63]
	v_pk_mul_f32 v[62:63], v[110:111], v[108:109]
	v_accvgpr_read_b32 v30, a6
	v_mov_b32_dpp v49, v120 row_shl:1 row_mask:0xf bank_mask:0xf
	v_pk_fma_f32 v[62:63], v[120:121], v[30:31], v[62:63] op_sel_hi:[0,1,1]
	v_mov_b32_e32 v68, v121
	v_mov_b32_e32 v69, v71
	v_pk_fma_f32 v[62:63], v[68:69], v[48:49], v[62:63]
	s_mov_b64 s[0:1], 0x430000
	v_pk_add_f32 v[60:61], v[60:61], v[62:63]
	v_lshl_add_u64 v[136:137], v[134:135], 0, s[0:1]
	v_add_u32_e32 v1, s16, v118
	s_add_u32 s0, s10, 0x1800000
	v_accvgpr_write_b32 a26, v114
	s_nop 1
	s_mov_b64 vcc, s[28:29]
	s_nop 0
	v_cndmask_b32_dpp v130, v60, v128, vcc quad_perm:[1,0,3,2] row_mask:0xf bank_mask:0xf
	v_cndmask_b32_dpp v131, v61, v129, vcc quad_perm:[1,0,3,2] row_mask:0xf bank_mask:0xf
	s_mov_b64 vcc, s[30:31]
	s_nop 0
	v_cndmask_b32_dpp v132, v128, v60, vcc quad_perm:[1,0,3,2] row_mask:0xf bank_mask:0xf
	v_cndmask_b32_dpp v133, v129, v61, vcc quad_perm:[1,0,3,2] row_mask:0xf bank_mask:0xf
	global_store_dwordx4 v[136:137], v[130:133], off sc0 sc1 nt
	s_nop 1
	v_readfirstlane_b32 s2, v1
	s_addc_u32 s1, s11, 0
	v_add_u32_e32 v1, s16, v90
	v_accvgpr_write_b32 a18, v116
	v_accvgpr_write_b32 a27, v115
	s_waitcnt vmcnt(16)
	v_lshl_add_u64 v[60:61], s[0:1], 0, v[32:33]
	s_mov_b32 m0, s2
	v_readfirstlane_b32 s2, v1
	v_add_u32_e32 v1, s16, v91
	v_accvgpr_read_b32 v115, a23
	v_accvgpr_write_b32 a19, v117
	s_waitcnt lgkmcnt(0)
	s_barrier
	global_load_lds_dwordx4 v[60:61], off nt
	v_lshl_add_u64 v[60:61], s[0:1], 0, v[74:75]
	s_mov_b32 m0, s2
	v_readfirstlane_b32 s2, v1
	v_accvgpr_read_b32 v114, a22
	v_add_u32_e32 v1, s16, v119
	v_accvgpr_read_b32 v117, a31
	global_load_lds_dwordx4 v[60:61], off nt
	v_lshl_add_u64 v[60:61], s[0:1], 0, v[114:115]
	s_mov_b32 m0, s2
	v_readfirstlane_b32 s2, v1
	v_accvgpr_read_b32 v116, a30
	global_load_lds_dwordx4 v[60:61], off nt
	v_lshl_add_u64 v[60:61], s[0:1], 0, v[116:117]
	s_mov_b32 m0, s2
	v_accvgpr_write_b32 a1, v5
	global_load_lds_dwordx4 v[60:61], off nt
	v_accvgpr_read_b32 v5, a10
	v_add_u32_e32 v2, 16, v5
	ds_read_b64 v[60:61], v2
	ds_read_b64 v[62:63], v2 offset:288
	ds_read_b64 v[68:69], v2 offset:576
	ds_read_b64 v[70:71], v2 offset:1728
	ds_read_b64 v[72:73], v2 offset:2016
	ds_read_b64 v[82:83], v2 offset:2304
	ds_read_b64 v[80:81], v2 offset:3456
	ds_read_b64 v[84:85], v2 offset:3744
	ds_read_b64 v[124:125], v2 offset:4032
	ds_read_b64 v[122:123], v2 offset:5184
	ds_read_b64 v[120:121], v2 offset:5472
	ds_read_b64 v[90:91], v2 offset:5760
	ds_read_b32 v43, v4
	ds_read_b32 v19, v4 offset:288
	ds_read_b32 v39, v4 offset:576
	ds_read_b32 v25, v4 offset:1728
	ds_read_b32 v7, v4 offset:2016
	ds_read_b32 v21, v4 offset:2304
	ds_read_b32 v11, v4 offset:3456
	ds_read_b32 v35, v4 offset:3744
	ds_read_b32 v59, v4 offset:4032
	ds_read_b32 v57, v4 offset:5184
	ds_read_b32 v51, v4 offset:5472
	ds_read_b32 v49, v4 offset:5760
	s_waitcnt lgkmcnt(0)
	v_accvgpr_write_b32 a46, v88
	v_mov_b32_e32 v46, v43
	v_accvgpr_write_b32 a8, v8
	v_mov_b32_e32 v113, v61
	v_mov_b32_dpp v46, v61 row_shr:1 row_mask:0xf bank_mask:0xf
	v_accvgpr_mov_b32 a42, a52
	v_accvgpr_write_b32 a47, v89
	v_accvgpr_write_b32 a9, v9
	v_pk_mul_f32 v[88:89], v[112:113], v[46:47]
	v_accvgpr_write_b32 a40, v112
	v_accvgpr_read_b32 v8, a18
	v_accvgpr_read_b32 v113, a39
	v_accvgpr_mov_b32 a43, a53
	v_accvgpr_write_b32 a51, v33
	v_accvgpr_write_b32 a52, v74
	v_accvgpr_read_b32 v9, a19
	v_accvgpr_read_b32 v112, a38
	v_mov_b32_e32 v26, v19
	v_accvgpr_write_b32 a50, v32
	v_accvgpr_write_b32 a53, v75
	v_mov_b32_dpp v43, v60 row_shl:1 row_mask:0xf bank_mask:0xf
	v_pk_fma_f32 v[88:89], v[60:61], v[8:9], v[88:89] op_sel_hi:[0,1,1]
	v_pk_mov_b32 v[60:61], v[60:61], v[112:113] op_sel:[1,0]
	v_mov_b32_dpp v26, v63 row_shr:1 row_mask:0xf bank_mask:0xf
	v_accvgpr_read_b32 v32, a34
	v_mov_b32_e32 v33, v63
	v_accvgpr_read_b32 v127, a27
	v_accvgpr_read_b32 v75, a43
	v_pk_fma_f32 v[60:61], v[60:61], v[42:43], v[88:89]
	v_pk_mul_f32 v[88:89], v[32:33], v[26:27]
	v_accvgpr_read_b32 v126, a26
	v_accvgpr_read_b32 v74, a42
	v_mov_b32_dpp v19, v62 row_shl:1 row_mask:0xf bank_mask:0xf
	v_pk_fma_f32 v[88:89], v[62:63], v[126:127], v[88:89] op_sel_hi:[0,1,1]
	v_pk_mov_b32 v[62:63], v[62:63], v[74:75] op_sel:[1,0]
	v_mov_b32_e32 v44, v39
	v_accvgpr_mov_b32 a14, a48
	v_pk_fma_f32 v[62:63], v[62:63], v[18:19], v[88:89]
	v_pk_add_f32 v[60:61], v[60:61], 0 op_sel_hi:[1,0]
	v_mov_b32_dpp v44, v69 row_shr:1 row_mask:0xf bank_mask:0xf
	v_mov_b32_e32 v1, v69
	v_accvgpr_mov_b32 a15, a49
	v_pk_add_f32 v[60:61], v[60:61], v[62:63]
	v_pk_mul_f32 v[62:63], v[0:1], v[44:45]
	v_accvgpr_write_b32 a48, v0
	v_accvgpr_read_b32 v89, a45
	v_accvgpr_read_b32 v0, a46
	v_accvgpr_read_b32 v88, a44
	v_accvgpr_read_b32 v1, a47
	v_mov_b32_dpp v39, v68 row_shl:1 row_mask:0xf bank_mask:0xf
	v_pk_fma_f32 v[62:63], v[68:69], v[88:89], v[62:63] op_sel_hi:[0,1,1]
	v_pk_mov_b32 v[68:69], v[68:69], v[0:1] op_sel:[1,0]
	v_mov_b32_e32 v36, v25
	v_pk_fma_f32 v[62:63], v[68:69], v[38:39], v[62:63]
	s_mov_b64 s[0:1], 0x800000
	v_pk_add_f32 v[60:61], v[60:61], v[62:63]
	v_mov_b32_dpp v36, v71 row_shr:1 row_mask:0xf bank_mask:0xf
	v_mov_b32_e32 v65, v71
	v_lshl_add_u64 v[62:63], v[54:55], 0, s[0:1]
	v_mov_b32_e32 v128, v60
	v_mov_b32_e32 v129, v61
	v_pk_mul_f32 v[60:61], v[64:65], v[36:37]
	v_mov_b64_e32 v[118:119], v[86:87]
	v_mov_b32_e32 v12, v7
	v_accvgpr_write_b32 a24, v32
	v_mov_b32_dpp v25, v70 row_shl:1 row_mask:0xf bank_mask:0xf
	v_pk_fma_f32 v[60:61], v[70:71], v[118:119], v[60:61] op_sel_hi:[0,1,1]
	v_mov_b32_e32 v62, v71
	v_mov_b32_e32 v63, v113
	v_mov_b32_dpp v12, v73 row_shr:1 row_mask:0xf bank_mask:0xf
	v_accvgpr_read_b32 v32, a20
	v_mov_b32_e32 v33, v73
	v_pk_fma_f32 v[60:61], v[62:63], v[24:25], v[60:61]
	v_pk_mul_f32 v[62:63], v[32:33], v[12:13]
	v_mov_b32_dpp v7, v72 row_shl:1 row_mask:0xf bank_mask:0xf
	v_pk_fma_f32 v[62:63], v[72:73], v[106:107], v[62:63] op_sel_hi:[0,1,1]
	v_mov_b32_e32 v68, v73
	v_mov_b32_e32 v69, v75
	v_mov_b32_e32 v78, v21
	v_pk_fma_f32 v[62:63], v[68:69], v[6:7], v[62:63]
	v_pk_add_f32 v[60:61], v[60:61], 0 op_sel_hi:[1,0]
	v_mov_b32_dpp v78, v83 row_shr:1 row_mask:0xf bank_mask:0xf
	v_mov_b32_e32 v53, v83
	v_pk_add_f32 v[60:61], v[60:61], v[62:63]
	v_pk_mul_f32 v[62:63], v[52:53], v[78:79]
	v_mov_b32_dpp v21, v82 row_shl:1 row_mask:0xf bank_mask:0xf
	v_pk_fma_f32 v[62:63], v[82:83], v[14:15], v[62:63] op_sel_hi:[0,1,1]
	v_mov_b32_e32 v68, v83
	v_mov_b32_e32 v69, v1
	v_accvgpr_write_b32 a19, v15
	v_pk_fma_f32 v[62:63], v[68:69], v[20:21], v[62:63]
	v_mov_b32_e32 v76, v11
	v_accvgpr_write_b32 a18, v14
	v_pk_add_f32 v[60:61], v[60:61], v[62:63]
	s_mov_b64 s[0:1], 0x810000
	v_mov_b32_dpp v76, v81 row_shr:1 row_mask:0xf bank_mask:0xf
	v_mov_b32_e32 v41, v81
	v_accvgpr_read_b32 v14, a36
	v_accvgpr_write_b32 a6, v2
	v_lshl_add_u64 v[136:137], v[134:135], 0, s[0:1]
	s_nop 1
	s_mov_b64 vcc, s[28:29]
	s_nop 0
	v_cndmask_b32_dpp v130, v60, v128, vcc quad_perm:[1,0,3,2] row_mask:0xf bank_mask:0xf
	v_cndmask_b32_dpp v131, v61, v129, vcc quad_perm:[1,0,3,2] row_mask:0xf bank_mask:0xf
	s_mov_b64 vcc, s[30:31]
	s_nop 0
	v_cndmask_b32_dpp v132, v128, v60, vcc quad_perm:[1,0,3,2] row_mask:0xf bank_mask:0xf
	v_cndmask_b32_dpp v133, v129, v61, vcc quad_perm:[1,0,3,2] row_mask:0xf bank_mask:0xf
	global_store_dwordx4 v[136:137], v[130:133], off sc0 sc1 nt
	s_nop 1
	v_pk_mul_f32 v[60:61], v[40:41], v[76:77]
	v_accvgpr_read_b32 v15, a37
	v_mov_b32_e32 v2, v35
	v_mov_b32_dpp v11, v80 row_shl:1 row_mask:0xf bank_mask:0xf
	v_pk_fma_f32 v[60:61], v[80:81], v[14:15], v[60:61] op_sel_hi:[0,1,1]
	v_pk_mov_b32 v[62:63], v[80:81], v[66:67] op_sel:[1,0]
	v_mov_b32_dpp v2, v85 row_shr:1 row_mask:0xf bank_mask:0xf
	v_mov_b32_e32 v23, v85
	v_accvgpr_read_b32 v15, a9
	v_pk_fma_f32 v[60:61], v[62:63], v[10:11], v[60:61]
	v_pk_mul_f32 v[62:63], v[22:23], v[2:3]
	v_accvgpr_read_b32 v14, a8
	v_mov_b32_dpp v35, v84 row_shl:1 row_mask:0xf bank_mask:0xf
	v_pk_fma_f32 v[62:63], v[84:85], v[100:101], v[62:63] op_sel_hi:[0,1,1]
	v_pk_mov_b32 v[68:69], v[84:85], v[14:15] op_sel:[1,0]
	v_mov_b32_e32 v92, v59
	v_pk_fma_f32 v[62:63], v[68:69], v[34:35], v[62:63]
	v_pk_add_f32 v[60:61], v[60:61], 0 op_sel_hi:[1,0]
	v_mov_b32_dpp v92, v125 row_shr:1 row_mask:0xf bank_mask:0xf
	v_mov_b32_e32 v97, v125
	v_accvgpr_read_b32 v71, a15
	v_pk_add_f32 v[60:61], v[60:61], v[62:63]
	v_pk_mul_f32 v[62:63], v[96:97], v[92:93]
	v_accvgpr_read_b32 v70, a14
	v_mov_b32_dpp v59, v124 row_shl:1 row_mask:0xf bank_mask:0xf
	v_pk_fma_f32 v[62:63], v[124:125], v[16:17], v[62:63] op_sel_hi:[0,1,1]
	v_pk_mov_b32 v[68:69], v[124:125], v[70:71] op_sel:[1,0]
	v_mov_b32_e32 v94, v57
	v_pk_fma_f32 v[62:63], v[68:69], v[58:59], v[62:63]
	s_mov_b64 s[0:1], 0x820000
	v_pk_add_f32 v[60:61], v[60:61], v[62:63]
	v_mov_b32_dpp v94, v123 row_shr:1 row_mask:0xf bank_mask:0xf
	v_mov_b32_e32 v99, v123
	v_accvgpr_write_b32 a31, v17
	v_lshl_add_u64 v[62:63], v[54:55], 0, s[0:1]
	v_mov_b32_e32 v128, v60
	v_mov_b32_e32 v129, v61
	v_pk_mul_f32 v[60:61], v[98:99], v[94:95]
	v_mov_b32_e32 v102, v51
	v_accvgpr_write_b32 a30, v16
	v_mov_b32_dpp v57, v122 row_shl:1 row_mask:0xf bank_mask:0xf
	v_pk_fma_f32 v[60:61], v[122:123], v[28:29], v[60:61] op_sel_hi:[0,1,1]
	v_mov_b32_e32 v62, v123
	v_mov_b32_e32 v63, v67
	v_mov_b32_dpp v102, v121 row_shr:1 row_mask:0xf bank_mask:0xf
	v_mov_b32_e32 v105, v121
	v_accvgpr_read_b32 v16, a28
	v_pk_fma_f32 v[60:61], v[62:63], v[56:57], v[60:61]
	v_pk_mul_f32 v[62:63], v[104:105], v[102:103]
	v_accvgpr_read_b32 v17, a29
	v_mov_b32_dpp v51, v120 row_shl:1 row_mask:0xf bank_mask:0xf
	v_pk_fma_f32 v[62:63], v[120:121], v[16:17], v[62:63] op_sel_hi:[0,1,1]
	v_mov_b32_e32 v68, v121
	v_mov_b32_e32 v69, v15
	v_mov_b32_e32 v108, v49
	v_pk_fma_f32 v[62:63], v[68:69], v[50:51], v[62:63]
	v_pk_add_f32 v[60:61], v[60:61], 0 op_sel_hi:[1,0]
	v_mov_b32_dpp v108, v91 row_shr:1 row_mask:0xf bank_mask:0xf
	v_mov_b32_e32 v111, v91
	v_pk_add_f32 v[60:61], v[60:61], v[62:63]
	v_pk_mul_f32 v[62:63], v[110:111], v[108:109]
	v_mov_b32_dpp v49, v90 row_shl:1 row_mask:0xf bank_mask:0xf
	v_pk_fma_f32 v[62:63], v[90:91], v[30:31], v[62:63] op_sel_hi:[0,1,1]
	v_mov_b32_e32 v68, v91
	v_mov_b32_e32 v69, v71
	v_pk_fma_f32 v[62:63], v[68:69], v[48:49], v[62:63]
	s_mov_b64 s[0:1], 0x830000
	v_mov_b32_e32 v0, v22
	v_pk_add_f32 v[60:61], v[60:61], v[62:63]
	v_lshl_add_u64 v[136:137], v[134:135], 0, s[0:1]
	s_add_u32 s0, s10, 0x1c00000
	v_accvgpr_read_b32 v22, a50
	v_accvgpr_read_b32 v1, a72
	s_addc_u32 s1, s11, 0
	v_accvgpr_read_b32 v23, a51
	s_nop 1
	s_mov_b64 vcc, s[28:29]
	s_nop 0
	v_cndmask_b32_dpp v130, v60, v128, vcc quad_perm:[1,0,3,2] row_mask:0xf bank_mask:0xf
	v_cndmask_b32_dpp v131, v61, v129, vcc quad_perm:[1,0,3,2] row_mask:0xf bank_mask:0xf
	s_mov_b64 vcc, s[30:31]
	s_nop 0
	v_cndmask_b32_dpp v132, v128, v60, vcc quad_perm:[1,0,3,2] row_mask:0xf bank_mask:0xf
	v_cndmask_b32_dpp v133, v129, v61, vcc quad_perm:[1,0,3,2] row_mask:0xf bank_mask:0xf
	global_store_dwordx4 v[136:137], v[130:133], off sc0 sc1 nt
	s_nop 1
	v_readfirstlane_b32 s2, v1
	v_lshl_add_u64 v[60:61], s[0:1], 0, v[22:23]
	v_accvgpr_read_b32 v1, a12
	v_accvgpr_read_b32 v22, a52
	s_waitcnt vmcnt(18)
	s_mov_b32 m0, s2
	v_readfirstlane_b32 s2, v1
	v_accvgpr_read_b32 v23, a53
	v_accvgpr_read_b32 v1, a13
	s_waitcnt lgkmcnt(0)
	s_barrier
	global_load_lds_dwordx4 v[60:61], off nt
	v_lshl_add_u64 v[60:61], s[0:1], 0, v[22:23]
	s_mov_b32 m0, s2
	v_readfirstlane_b32 s2, v1
	v_accvgpr_read_b32 v1, a16
	global_load_lds_dwordx4 v[60:61], off nt
	v_lshl_add_u64 v[60:61], s[0:1], 0, v[114:115]
	s_mov_b32 m0, s2
	v_readfirstlane_b32 s2, v1
	global_load_lds_dwordx4 v[60:61], off nt
	v_lshl_add_u64 v[60:61], s[0:1], 0, v[116:117]
	s_mov_b32 m0, s2
	v_accvgpr_write_b32 a22, v30
	v_accvgpr_write_b32 a44, v70
	global_load_lds_dwordx4 v[60:61], off nt
	v_accvgpr_write_b32 a2, v106
	v_accvgpr_write_b32 a34, v74
	v_accvgpr_write_b32 a23, v31
	v_accvgpr_write_b32 a45, v71
	v_add_u32_e32 v2, 0x7010, v5
	v_mov_b32_e32 v31, v5
	v_add_u32_e32 v5, 0x7000, v4
	ds_read_b64 v[60:61], v2
	ds_read_b64 v[62:63], v2 offset:288
	ds_read_b64 v[68:69], v2 offset:576
	ds_read_b64 v[70:71], v2 offset:1728
	ds_read_b64 v[72:73], v2 offset:2016
	ds_read_b64 v[82:83], v2 offset:2304
	ds_read_b64 v[80:81], v2 offset:3456
	ds_read_b64 v[84:85], v2 offset:3744
	ds_read_b64 v[116:117], v2 offset:4032
	ds_read_b64 v[114:115], v2 offset:5184
	ds_read_b64 v[112:113], v2 offset:5472
	ds_read_b64 v[90:91], v2 offset:5760
	ds_read_b32 v43, v5
	ds_read_b32 v19, v5 offset:288
	ds_read_b32 v39, v5 offset:576
	ds_read_b32 v25, v5 offset:1728
	ds_read_b32 v7, v5 offset:2016
	ds_read_b32 v21, v5 offset:2304
	ds_read_b32 v11, v5 offset:3456
	ds_read_b32 v35, v5 offset:3744
	ds_read_b32 v59, v5 offset:4032
	ds_read_b32 v57, v5 offset:5184
	ds_read_b32 v51, v5 offset:5472
	ds_read_b32 v49, v5 offset:5760
	s_waitcnt lgkmcnt(0)
	v_accvgpr_write_b32 a3, v107
	v_mov_b32_e32 v46, v43
	v_accvgpr_write_b32 a35, v75
	v_accvgpr_read_b32 v74, a40
	v_mov_b32_dpp v46, v61 row_shr:1 row_mask:0xf bank_mask:0xf
	v_mov_b32_e32 v75, v61
	v_accvgpr_read_b32 v107, a39
	v_accvgpr_write_b32 a10, v100
	v_pk_mul_f32 v[86:87], v[74:75], v[46:47]
	v_accvgpr_read_b32 v106, a38
	v_mov_b32_e32 v26, v19
	v_accvgpr_write_b32 a11, v101
	v_mov_b32_dpp v43, v60 row_shl:1 row_mask:0xf bank_mask:0xf
	v_mov_b32_e32 v32, v74
	v_pk_fma_f32 v[86:87], v[60:61], v[8:9], v[86:87] op_sel_hi:[0,1,1]
	v_pk_mov_b32 v[60:61], v[60:61], v[106:107] op_sel:[1,0]
	v_mov_b32_dpp v26, v63 row_shr:1 row_mask:0xf bank_mask:0xf
	v_accvgpr_read_b32 v74, a24
	v_mov_b32_e32 v75, v63
	v_accvgpr_read_b32 v101, a35
	v_pk_fma_f32 v[60:61], v[60:61], v[42:43], v[86:87]
	v_pk_mul_f32 v[86:87], v[74:75], v[26:27]
	v_accvgpr_read_b32 v100, a34
	v_accvgpr_write_b32 a14, v66
	v_mov_b32_dpp v19, v62 row_shl:1 row_mask:0xf bank_mask:0xf
	v_pk_fma_f32 v[86:87], v[62:63], v[126:127], v[86:87] op_sel_hi:[0,1,1]
	v_pk_mov_b32 v[62:63], v[62:63], v[100:101] op_sel:[1,0]
	v_mov_b32_e32 v44, v39
	v_accvgpr_write_b32 a42, v64
	v_accvgpr_write_b32 a15, v67
	v_mov_b32_e32 v66, v4
	v_pk_fma_f32 v[62:63], v[62:63], v[18:19], v[86:87]
	v_pk_add_f32 v[60:61], v[60:61], 0 op_sel_hi:[1,0]
	v_mov_b32_dpp v44, v69 row_shr:1 row_mask:0xf bank_mask:0xf
	v_accvgpr_read_b32 v64, a48
	v_mov_b32_e32 v65, v69
	v_accvgpr_read_b32 v4, a46
	v_pk_add_f32 v[60:61], v[60:61], v[62:63]
	v_pk_mul_f32 v[62:63], v[64:65], v[44:45]
	v_accvgpr_read_b32 v5, a47
	v_mov_b32_dpp v39, v68 row_shl:1 row_mask:0xf bank_mask:0xf
	v_pk_fma_f32 v[62:63], v[68:69], v[88:89], v[62:63] op_sel_hi:[0,1,1]
	v_pk_mov_b32 v[68:69], v[68:69], v[4:5] op_sel:[1,0]
	v_mov_b32_e32 v36, v25
	v_pk_fma_f32 v[62:63], v[68:69], v[38:39], v[62:63]
	s_mov_b64 s[0:1], 0xc00000
	v_pk_add_f32 v[60:61], v[60:61], v[62:63]
	v_mov_b32_dpp v36, v71 row_shr:1 row_mask:0xf bank_mask:0xf
	v_accvgpr_read_b32 v22, a42
	v_mov_b32_e32 v23, v71
	v_accvgpr_mov_b32 a26, a20
	v_accvgpr_write_b32 a20, v28
	v_lshl_add_u64 v[62:63], v[54:55], 0, s[0:1]
	v_mov_b32_e32 v128, v60
	v_mov_b32_e32 v129, v61
	v_pk_mul_f32 v[60:61], v[22:23], v[36:37]
	v_mov_b32_e32 v12, v7
	v_accvgpr_write_b32 a21, v29
	v_mov_b32_dpp v25, v70 row_shl:1 row_mask:0xf bank_mask:0xf
	v_pk_fma_f32 v[60:61], v[70:71], v[118:119], v[60:61] op_sel_hi:[0,1,1]
	v_mov_b32_e32 v62, v71
	v_mov_b32_e32 v63, v107
	v_mov_b32_dpp v12, v73 row_shr:1 row_mask:0xf bank_mask:0xf
	v_accvgpr_read_b32 v28, a26
	v_mov_b32_e32 v29, v73
	v_accvgpr_read_b32 v121, a3
	v_pk_fma_f32 v[60:61], v[62:63], v[24:25], v[60:61]
	v_pk_mul_f32 v[62:63], v[28:29], v[12:13]
	v_accvgpr_read_b32 v120, a2
	v_mov_b32_dpp v7, v72 row_shl:1 row_mask:0xf bank_mask:0xf
	v_pk_fma_f32 v[62:63], v[72:73], v[120:121], v[62:63] op_sel_hi:[0,1,1]
	v_mov_b32_e32 v68, v73
	v_mov_b32_e32 v69, v101
	v_mov_b32_e32 v78, v21
	v_pk_fma_f32 v[62:63], v[68:69], v[6:7], v[62:63]
	v_pk_add_f32 v[60:61], v[60:61], 0 op_sel_hi:[1,0]
	v_mov_b32_dpp v78, v83 row_shr:1 row_mask:0xf bank_mask:0xf
	v_mov_b32_e32 v53, v83
	v_accvgpr_read_b32 v125, a19
	v_pk_add_f32 v[60:61], v[60:61], v[62:63]
	v_pk_mul_f32 v[62:63], v[52:53], v[78:79]
	v_accvgpr_read_b32 v124, a18
	v_mov_b32_dpp v21, v82 row_shl:1 row_mask:0xf bank_mask:0xf
	v_pk_fma_f32 v[62:63], v[82:83], v[124:125], v[62:63] op_sel_hi:[0,1,1]
	v_mov_b32_e32 v68, v83
	v_mov_b32_e32 v69, v5
	v_pk_fma_f32 v[62:63], v[68:69], v[20:21], v[62:63]
	v_mov_b32_e32 v76, v11
	v_pk_add_f32 v[60:61], v[60:61], v[62:63]
	s_mov_b64 s[0:1], 0xc10000
	v_mov_b32_dpp v76, v81 row_shr:1 row_mask:0xf bank_mask:0xf
	v_mov_b32_e32 v41, v81
	v_accvgpr_read_b32 v123, a37
	v_accvgpr_read_b32 v4, a14
	v_lshl_add_u64 v[136:137], v[134:135], 0, s[0:1]
	s_nop 1
	s_mov_b64 vcc, s[28:29]
	s_nop 0
	v_cndmask_b32_dpp v130, v60, v128, vcc quad_perm:[1,0,3,2] row_mask:0xf bank_mask:0xf
	v_cndmask_b32_dpp v131, v61, v129, vcc quad_perm:[1,0,3,2] row_mask:0xf bank_mask:0xf
	s_mov_b64 vcc, s[30:31]
	s_nop 0
	v_cndmask_b32_dpp v132, v128, v60, vcc quad_perm:[1,0,3,2] row_mask:0xf bank_mask:0xf
	v_cndmask_b32_dpp v133, v129, v61, vcc quad_perm:[1,0,3,2] row_mask:0xf bank_mask:0xf
	global_store_dwordx4 v[136:137], v[130:133], off sc0 sc1 nt
	s_nop 1
	v_pk_mul_f32 v[60:61], v[40:41], v[76:77]
	v_accvgpr_read_b32 v122, a36
	v_accvgpr_read_b32 v5, a15
	v_mov_b32_e32 v2, v35
	v_accvgpr_mov_b32 a32, a24
	v_accvgpr_write_b32 a24, v22
	v_mov_b64_e32 v[22:23], v[118:119]
	v_mov_b32_dpp v11, v80 row_shl:1 row_mask:0xf bank_mask:0xf
	v_pk_fma_f32 v[60:61], v[80:81], v[122:123], v[60:61] op_sel_hi:[0,1,1]
	v_pk_mov_b32 v[62:63], v[80:81], v[4:5] op_sel:[1,0]
	v_mov_b32_dpp v2, v85 row_shr:1 row_mask:0xf bank_mask:0xf
	v_mov_b32_e32 v106, v0
	v_mov_b32_e32 v107, v85
	v_accvgpr_read_b32 v119, a11
	v_pk_fma_f32 v[60:61], v[62:63], v[10:11], v[60:61]
	v_pk_mul_f32 v[62:63], v[106:107], v[2:3]
	v_accvgpr_read_b32 v118, a10
	v_mov_b64_e32 v[100:101], v[14:15]
	v_mov_b32_dpp v35, v84 row_shl:1 row_mask:0xf bank_mask:0xf
	v_pk_fma_f32 v[62:63], v[84:85], v[118:119], v[62:63] op_sel_hi:[0,1,1]
	v_pk_mov_b32 v[68:69], v[84:85], v[100:101] op_sel:[1,0]
	v_mov_b32_e32 v92, v59
	v_accvgpr_write_b32 a26, v52
	v_mov_b32_e32 v74, v40
	v_pk_fma_f32 v[62:63], v[68:69], v[34:35], v[62:63]
	v_pk_add_f32 v[60:61], v[60:61], 0 op_sel_hi:[1,0]
	v_mov_b32_dpp v92, v117 row_shr:1 row_mask:0xf bank_mask:0xf
	v_mov_b32_e32 v97, v117
	v_accvgpr_read_b32 v41, a31
	v_accvgpr_read_b32 v53, a45
	v_pk_add_f32 v[60:61], v[60:61], v[62:63]
	v_pk_mul_f32 v[62:63], v[96:97], v[92:93]
	v_accvgpr_read_b32 v40, a30
	v_accvgpr_read_b32 v52, a44
	v_mov_b32_dpp v59, v116 row_shl:1 row_mask:0xf bank_mask:0xf
	v_pk_fma_f32 v[62:63], v[116:117], v[40:41], v[62:63] op_sel_hi:[0,1,1]
	v_pk_mov_b32 v[68:69], v[116:117], v[52:53] op_sel:[1,0]
	v_mov_b32_e32 v94, v57
	v_pk_fma_f32 v[62:63], v[68:69], v[58:59], v[62:63]
	s_mov_b64 s[0:1], 0xc20000
	v_pk_add_f32 v[60:61], v[60:61], v[62:63]
	v_mov_b32_dpp v94, v115 row_shr:1 row_mask:0xf bank_mask:0xf
	v_mov_b32_e32 v99, v115
	v_accvgpr_read_b32 v14, a20
	v_lshl_add_u64 v[62:63], v[54:55], 0, s[0:1]
	v_mov_b32_e32 v128, v60
	v_mov_b32_e32 v129, v61
	v_pk_mul_f32 v[60:61], v[98:99], v[94:95]
	v_accvgpr_read_b32 v15, a21
	v_mov_b32_e32 v102, v51
	v_mov_b32_dpp v57, v114 row_shl:1 row_mask:0xf bank_mask:0xf
	v_pk_fma_f32 v[60:61], v[114:115], v[14:15], v[60:61] op_sel_hi:[0,1,1]
	v_mov_b32_e32 v62, v115
	v_mov_b32_e32 v63, v5
	v_mov_b32_dpp v102, v113 row_shr:1 row_mask:0xf bank_mask:0xf
	v_mov_b32_e32 v105, v113
	v_pk_fma_f32 v[60:61], v[62:63], v[56:57], v[60:61]
	v_pk_mul_f32 v[62:63], v[104:105], v[102:103]
	v_accvgpr_write_b32 a8, v8
	v_mov_b32_dpp v51, v112 row_shl:1 row_mask:0xf bank_mask:0xf
	v_pk_fma_f32 v[62:63], v[112:113], v[16:17], v[62:63] op_sel_hi:[0,1,1]
	v_mov_b32_e32 v68, v113
	v_mov_b32_e32 v69, v101
	v_mov_b32_e32 v108, v49
	v_accvgpr_write_b32 a9, v9
	v_pk_fma_f32 v[62:63], v[68:69], v[50:51], v[62:63]
	v_pk_add_f32 v[60:61], v[60:61], 0 op_sel_hi:[1,0]
	v_mov_b32_dpp v108, v91 row_shr:1 row_mask:0xf bank_mask:0xf
	v_mov_b32_e32 v111, v91
	v_accvgpr_read_b32 v8, a22
	v_pk_add_f32 v[60:61], v[60:61], v[62:63]
	v_pk_mul_f32 v[62:63], v[110:111], v[108:109]
	v_accvgpr_read_b32 v9, a23
	v_mov_b32_dpp v49, v90 row_shl:1 row_mask:0xf bank_mask:0xf
	v_pk_fma_f32 v[62:63], v[90:91], v[8:9], v[62:63] op_sel_hi:[0,1,1]
	v_mov_b32_e32 v68, v91
	v_mov_b32_e32 v69, v53
	v_pk_fma_f32 v[62:63], v[68:69], v[48:49], v[62:63]
	s_mov_b64 s[0:1], 0xc30000
	v_pk_add_f32 v[60:61], v[60:61], v[62:63]
	v_lshl_add_u64 v[136:137], v[134:135], 0, s[0:1]
	s_nop 1
	s_mov_b64 vcc, s[28:29]
	s_nop 0
	v_cndmask_b32_dpp v130, v60, v128, vcc quad_perm:[1,0,3,2] row_mask:0xf bank_mask:0xf
	v_cndmask_b32_dpp v131, v61, v129, vcc quad_perm:[1,0,3,2] row_mask:0xf bank_mask:0xf
	s_mov_b64 vcc, s[30:31]
	s_nop 0
	v_cndmask_b32_dpp v132, v128, v60, vcc quad_perm:[1,0,3,2] row_mask:0xf bank_mask:0xf
	v_cndmask_b32_dpp v133, v129, v61, vcc quad_perm:[1,0,3,2] row_mask:0xf bank_mask:0xf
	global_store_dwordx4 v[136:137], v[130:133], off sc0 sc1 nt
	s_nop 1
	s_waitcnt vmcnt(20)
	v_accvgpr_write_b32 a16, v88
	v_accvgpr_write_b32 a10, v100
	s_waitcnt lgkmcnt(0)
	s_barrier
	v_add_u32_e32 v2, 0xe010, v31
	v_add_u32_e32 v5, 0xe000, v66
	ds_read_b64 v[60:61], v2
	ds_read_b64 v[62:63], v2 offset:288
	ds_read_b64 v[68:69], v2 offset:576
	ds_read_b64 v[70:71], v2 offset:1728
	ds_read_b64 v[72:73], v2 offset:2016
	ds_read_b64 v[82:83], v2 offset:2304
	ds_read_b64 v[80:81], v2 offset:3456
	ds_read_b64 v[84:85], v2 offset:3744
	ds_read_b64 v[116:117], v2 offset:4032
	ds_read_b64 v[114:115], v2 offset:5184
	ds_read_b64 v[112:113], v2 offset:5472
	ds_read_b64 v[90:91], v2 offset:5760
	ds_read_b32 v43, v5
	ds_read_b32 v19, v5 offset:288
	ds_read_b32 v39, v5 offset:576
	ds_read_b32 v25, v5 offset:1728
	ds_read_b32 v7, v5 offset:2016
	ds_read_b32 v21, v5 offset:2304
	ds_read_b32 v11, v5 offset:3456
	ds_read_b32 v35, v5 offset:3744
	ds_read_b32 v59, v5 offset:4032
	ds_read_b32 v57, v5 offset:5184
	ds_read_b32 v51, v5 offset:5472
	ds_read_b32 v49, v5 offset:5760
	s_waitcnt lgkmcnt(0)
	v_accvgpr_write_b32 a17, v89
	v_mov_b32_e32 v46, v43
	v_accvgpr_write_b32 a11, v101
	v_mov_b32_e32 v33, v61
	v_mov_b32_dpp v46, v61 row_shr:1 row_mask:0xf bank_mask:0xf
	v_accvgpr_read_b32 v89, a9
	v_accvgpr_read_b32 v101, a39
	v_pk_mul_f32 v[86:87], v[32:33], v[46:47]
	v_accvgpr_read_b32 v88, a8
	v_accvgpr_read_b32 v100, a38
	v_mov_b32_e32 v26, v19
	v_accvgpr_write_b32 a19, v17
	v_mov_b32_dpp v43, v60 row_shl:1 row_mask:0xf bank_mask:0xf
	v_pk_fma_f32 v[86:87], v[60:61], v[88:89], v[86:87] op_sel_hi:[0,1,1]
	v_pk_mov_b32 v[60:61], v[60:61], v[100:101] op_sel:[1,0]
	v_mov_b32_dpp v26, v63 row_shr:1 row_mask:0xf bank_mask:0xf
	v_accvgpr_read_b32 v0, a32
	v_mov_b32_e32 v1, v63
	v_accvgpr_read_b32 v4, a34
	v_accvgpr_write_b32 a18, v16
	v_pk_fma_f32 v[60:61], v[60:61], v[42:43], v[86:87]
	v_pk_mul_f32 v[86:87], v[0:1], v[26:27]
	v_mov_b64_e32 v[16:17], v[126:127]
	v_accvgpr_read_b32 v5, a35
	v_mov_b32_dpp v19, v62 row_shl:1 row_mask:0xf bank_mask:0xf
	v_pk_fma_f32 v[86:87], v[62:63], v[16:17], v[86:87] op_sel_hi:[0,1,1]
	v_pk_mov_b32 v[62:63], v[62:63], v[4:5] op_sel:[1,0]
	v_mov_b32_e32 v44, v39
	v_accvgpr_read_b32 v30, a48
	v_mov_b32_e32 v64, v28
	v_accvgpr_write_b32 a7, v66
	v_pk_fma_f32 v[62:63], v[62:63], v[18:19], v[86:87]
	v_pk_add_f32 v[60:61], v[60:61], 0 op_sel_hi:[1,0]
	v_mov_b32_dpp v44, v69 row_shr:1 row_mask:0xf bank_mask:0xf
	v_mov_b32_e32 v31, v69
	v_accvgpr_read_b32 v29, a17
	v_accvgpr_read_b32 v67, a47
	v_pk_add_f32 v[60:61], v[60:61], v[62:63]
	v_pk_mul_f32 v[62:63], v[30:31], v[44:45]
	v_accvgpr_read_b32 v28, a16
	v_accvgpr_read_b32 v66, a46
	v_mov_b32_dpp v39, v68 row_shl:1 row_mask:0xf bank_mask:0xf
	v_pk_fma_f32 v[62:63], v[68:69], v[28:29], v[62:63] op_sel_hi:[0,1,1]
	v_pk_mov_b32 v[68:69], v[68:69], v[66:67] op_sel:[1,0]
	v_mov_b32_e32 v36, v25
	v_pk_fma_f32 v[62:63], v[68:69], v[38:39], v[62:63]
	s_mov_b64 s[0:1], 0x1000000
	v_pk_add_f32 v[60:61], v[60:61], v[62:63]
	v_mov_b32_dpp v36, v71 row_shr:1 row_mask:0xf bank_mask:0xf
	v_accvgpr_read_b32 v126, a24
	v_mov_b32_e32 v127, v71
	v_lshl_add_u64 v[62:63], v[54:55], 0, s[0:1]
	v_mov_b32_e32 v128, v60
	v_mov_b32_e32 v129, v61
	v_pk_mul_f32 v[60:61], v[126:127], v[36:37]
	v_mov_b32_e32 v12, v7
	v_mov_b32_dpp v25, v70 row_shl:1 row_mask:0xf bank_mask:0xf
	v_pk_fma_f32 v[60:61], v[70:71], v[22:23], v[60:61] op_sel_hi:[0,1,1]
	v_mov_b32_e32 v62, v71
	v_mov_b32_e32 v63, v101
	v_mov_b32_dpp v12, v73 row_shr:1 row_mask:0xf bank_mask:0xf
	v_mov_b32_e32 v52, v64
	v_mov_b32_e32 v53, v73
	v_pk_fma_f32 v[60:61], v[62:63], v[24:25], v[60:61]
	v_pk_mul_f32 v[62:63], v[52:53], v[12:13]
	v_mov_b32_dpp v7, v72 row_shl:1 row_mask:0xf bank_mask:0xf
	v_pk_fma_f32 v[62:63], v[72:73], v[120:121], v[62:63] op_sel_hi:[0,1,1]
	v_mov_b32_e32 v68, v73
	v_mov_b32_e32 v69, v5
	v_mov_b32_e32 v78, v21
	v_pk_fma_f32 v[62:63], v[68:69], v[6:7], v[62:63]
	v_pk_add_f32 v[60:61], v[60:61], 0 op_sel_hi:[1,0]
	v_mov_b32_dpp v78, v83 row_shr:1 row_mask:0xf bank_mask:0xf
	v_accvgpr_read_b32 v4, a26
	v_mov_b32_e32 v5, v83
	v_pk_add_f32 v[60:61], v[60:61], v[62:63]
	v_pk_mul_f32 v[62:63], v[4:5], v[78:79]
	v_mov_b32_dpp v21, v82 row_shl:1 row_mask:0xf bank_mask:0xf
	v_pk_fma_f32 v[62:63], v[82:83], v[124:125], v[62:63] op_sel_hi:[0,1,1]
	v_mov_b32_e32 v68, v83
	v_mov_b32_e32 v69, v67
	v_accvgpr_write_b32 a8, v120
	v_pk_fma_f32 v[62:63], v[68:69], v[20:21], v[62:63]
	v_mov_b32_e32 v76, v11
	v_accvgpr_write_b32 a9, v121
	v_pk_add_f32 v[60:61], v[60:61], v[62:63]
	s_mov_b64 s[0:1], 0x1010000
	v_mov_b32_dpp v76, v81 row_shr:1 row_mask:0xf bank_mask:0xf
	v_mov_b32_e32 v120, v74
	v_mov_b32_e32 v121, v81
	v_accvgpr_read_b32 v101, a15
	v_accvgpr_mov_b32 a12, a38
	v_lshl_add_u64 v[136:137], v[134:135], 0, s[0:1]
	s_nop 1
	s_mov_b64 vcc, s[28:29]
	s_nop 0
	v_cndmask_b32_dpp v130, v60, v128, vcc quad_perm:[1,0,3,2] row_mask:0xf bank_mask:0xf
	v_cndmask_b32_dpp v131, v61, v129, vcc quad_perm:[1,0,3,2] row_mask:0xf bank_mask:0xf
	s_mov_b64 vcc, s[30:31]
	s_nop 0
	v_cndmask_b32_dpp v132, v128, v60, vcc quad_perm:[1,0,3,2] row_mask:0xf bank_mask:0xf
	v_cndmask_b32_dpp v133, v129, v61, vcc quad_perm:[1,0,3,2] row_mask:0xf bank_mask:0xf
	global_store_dwordx4 v[136:137], v[130:133], off sc0 sc1 nt
	s_nop 1
	v_pk_mul_f32 v[60:61], v[120:121], v[76:77]
	v_accvgpr_read_b32 v100, a14
	v_mov_b32_e32 v2, v35
	v_accvgpr_mov_b32 a13, a39
	v_accvgpr_write_b32 a20, v22
	v_mov_b32_dpp v11, v80 row_shl:1 row_mask:0xf bank_mask:0xf
	v_pk_fma_f32 v[60:61], v[80:81], v[122:123], v[60:61] op_sel_hi:[0,1,1]
	v_pk_mov_b32 v[62:63], v[80:81], v[100:101] op_sel:[1,0]
	v_mov_b32_dpp v2, v85 row_shr:1 row_mask:0xf bank_mask:0xf
	v_mov_b32_e32 v107, v85
	v_accvgpr_read_b32 v123, a11
	v_accvgpr_write_b32 a21, v23
	v_accvgpr_read_b32 v23, a13
	v_pk_fma_f32 v[60:61], v[62:63], v[10:11], v[60:61]
	v_pk_mul_f32 v[62:63], v[106:107], v[2:3]
	v_accvgpr_read_b32 v122, a10
	v_accvgpr_read_b32 v22, a12
	v_mov_b32_dpp v35, v84 row_shl:1 row_mask:0xf bank_mask:0xf
	v_pk_fma_f32 v[62:63], v[84:85], v[118:119], v[62:63] op_sel_hi:[0,1,1]
	v_accvgpr_write_b32 a12, v118
	v_pk_mov_b32 v[68:69], v[84:85], v[122:123] op_sel:[1,0]
	v_mov_b32_e32 v92, v59
	v_accvgpr_write_b32 a13, v119
	v_pk_fma_f32 v[62:63], v[68:69], v[34:35], v[62:63]
	v_pk_add_f32 v[60:61], v[60:61], 0 op_sel_hi:[1,0]
	v_mov_b32_dpp v92, v117 row_shr:1 row_mask:0xf bank_mask:0xf
	v_mov_b32_e32 v97, v117
	v_mov_b64_e32 v[118:119], v[40:41]
	v_accvgpr_read_b32 v40, a44
	v_pk_add_f32 v[60:61], v[60:61], v[62:63]
	v_pk_mul_f32 v[62:63], v[96:97], v[92:93]
	v_accvgpr_read_b32 v41, a45
	v_mov_b32_dpp v59, v116 row_shl:1 row_mask:0xf bank_mask:0xf
	v_pk_fma_f32 v[62:63], v[116:117], v[118:119], v[62:63] op_sel_hi:[0,1,1]
	v_pk_mov_b32 v[68:69], v[116:117], v[40:41] op_sel:[1,0]
	v_mov_b32_e32 v94, v57
	v_pk_fma_f32 v[62:63], v[68:69], v[58:59], v[62:63]
	s_mov_b64 s[0:1], 0x1020000
	v_pk_add_f32 v[60:61], v[60:61], v[62:63]
	v_mov_b32_dpp v94, v115 row_shr:1 row_mask:0xf bank_mask:0xf
	v_mov_b32_e32 v99, v115
	v_lshl_add_u64 v[62:63], v[54:55], 0, s[0:1]
	v_mov_b32_e32 v128, v60
	v_mov_b32_e32 v129, v61
	v_pk_mul_f32 v[60:61], v[98:99], v[94:95]
	v_mov_b32_e32 v102, v51
	v_accvgpr_write_b32 a30, v4
	v_mov_b32_dpp v57, v114 row_shl:1 row_mask:0xf bank_mask:0xf
	v_pk_fma_f32 v[60:61], v[114:115], v[14:15], v[60:61] op_sel_hi:[0,1,1]
	v_mov_b32_e32 v62, v115
	v_mov_b32_e32 v63, v101
	v_mov_b32_dpp v102, v113 row_shr:1 row_mask:0xf bank_mask:0xf
	v_mov_b32_e32 v105, v113
	v_accvgpr_read_b32 v4, a18
	v_pk_fma_f32 v[60:61], v[62:63], v[56:57], v[60:61]
	v_pk_mul_f32 v[62:63], v[104:105], v[102:103]
	v_accvgpr_read_b32 v5, a19
	v_mov_b32_dpp v51, v112 row_shl:1 row_mask:0xf bank_mask:0xf
	v_pk_fma_f32 v[62:63], v[112:113], v[4:5], v[62:63] op_sel_hi:[0,1,1]
	v_mov_b32_e32 v68, v113
	v_mov_b32_e32 v69, v123
	v_mov_b32_e32 v108, v49
	v_pk_fma_f32 v[62:63], v[68:69], v[50:51], v[62:63]
	v_pk_add_f32 v[60:61], v[60:61], 0 op_sel_hi:[1,0]
	v_mov_b32_dpp v108, v91 row_shr:1 row_mask:0xf bank_mask:0xf
	v_mov_b32_e32 v111, v91
	v_pk_add_f32 v[60:61], v[60:61], v[62:63]
	v_pk_mul_f32 v[62:63], v[110:111], v[108:109]
	v_mov_b32_dpp v49, v90 row_shl:1 row_mask:0xf bank_mask:0xf
	v_pk_fma_f32 v[62:63], v[90:91], v[8:9], v[62:63] op_sel_hi:[0,1,1]
	v_mov_b32_e32 v68, v91
	v_mov_b32_e32 v69, v41
	v_pk_fma_f32 v[62:63], v[68:69], v[48:49], v[62:63]
	s_mov_b64 s[0:1], 0x1030000
	v_pk_add_f32 v[60:61], v[60:61], v[62:63]
	v_lshl_add_u64 v[136:137], v[134:135], 0, s[0:1]
	s_nop 1
	s_mov_b64 vcc, s[28:29]
	s_nop 0
	v_cndmask_b32_dpp v130, v60, v128, vcc quad_perm:[1,0,3,2] row_mask:0xf bank_mask:0xf
	v_cndmask_b32_dpp v131, v61, v129, vcc quad_perm:[1,0,3,2] row_mask:0xf bank_mask:0xf
	s_mov_b64 vcc, s[30:31]
	s_nop 0
	v_cndmask_b32_dpp v132, v128, v60, vcc quad_perm:[1,0,3,2] row_mask:0xf bank_mask:0xf
	v_cndmask_b32_dpp v133, v129, v61, vcc quad_perm:[1,0,3,2] row_mask:0xf bank_mask:0xf
	global_store_dwordx4 v[136:137], v[130:133], off sc0 sc1 nt
	s_nop 1
	s_waitcnt vmcnt(16)
	s_waitcnt lgkmcnt(0)
	s_barrier
	v_accvgpr_read_b32 v2, a0
	v_accvgpr_read_b32 v8, a4
	ds_read_b64 v[60:61], v8
	ds_read_b64 v[62:63], v8 offset:288
	ds_read_b64 v[68:69], v8 offset:576
	ds_read_b64 v[70:71], v8 offset:1728
	ds_read_b64 v[72:73], v8 offset:2016
	ds_read_b64 v[82:83], v8 offset:2304
	ds_read_b64 v[80:81], v8 offset:3456
	ds_read_b64 v[84:85], v8 offset:3744
	ds_read_b64 v[116:117], v8 offset:4032
	ds_read_b64 v[114:115], v8 offset:5184
	ds_read_b64 v[112:113], v8 offset:5472
	ds_read_b64 v[90:91], v8 offset:5760
	ds_read_b32 v43, v2
	ds_read_b32 v19, v2 offset:288
	ds_read_b32 v39, v2 offset:576
	ds_read_b32 v25, v2 offset:1728
	ds_read_b32 v7, v2 offset:2016
	ds_read_b32 v21, v2 offset:2304
	ds_read_b32 v11, v2 offset:3456
	ds_read_b32 v35, v2 offset:3744
	ds_read_b32 v59, v2 offset:4032
	ds_read_b32 v57, v2 offset:5184
	ds_read_b32 v51, v2 offset:5472
	ds_read_b32 v49, v2 offset:5760
	s_waitcnt lgkmcnt(0)
	v_mov_b32_e32 v64, v32
	v_mov_b32_e32 v46, v43
	v_mov_b32_e32 v65, v61
	v_mov_b64_e32 v[100:101], v[22:23]
	v_mov_b32_dpp v46, v61 row_shr:1 row_mask:0xf bank_mask:0xf
	v_pk_mul_f32 v[86:87], v[64:65], v[46:47]
	v_mov_b32_e32 v26, v19
	v_mov_b32_dpp v43, v60 row_shl:1 row_mask:0xf bank_mask:0xf
	v_pk_fma_f32 v[86:87], v[60:61], v[88:89], v[86:87] op_sel_hi:[0,1,1]
	v_pk_mov_b32 v[60:61], v[60:61], v[100:101] op_sel:[1,0]
	v_mov_b32_dpp v26, v63 row_shr:1 row_mask:0xf bank_mask:0xf
	v_mov_b32_e32 v1, v63
	v_accvgpr_read_b32 v67, a35
	v_pk_fma_f32 v[60:61], v[60:61], v[42:43], v[86:87]
	v_pk_mul_f32 v[86:87], v[0:1], v[26:27]
	v_accvgpr_read_b32 v66, a34
	v_accvgpr_write_b32 a10, v14
	v_mov_b32_dpp v19, v62 row_shl:1 row_mask:0xf bank_mask:0xf
	v_pk_fma_f32 v[86:87], v[62:63], v[16:17], v[86:87] op_sel_hi:[0,1,1]
	v_pk_mov_b32 v[62:63], v[62:63], v[66:67] op_sel:[1,0]
	v_mov_b32_e32 v44, v39
	v_accvgpr_write_b32 a11, v15
	v_pk_fma_f32 v[62:63], v[62:63], v[18:19], v[86:87]
	v_pk_add_f32 v[60:61], v[60:61], 0 op_sel_hi:[1,0]
	v_mov_b32_dpp v44, v69 row_shr:1 row_mask:0xf bank_mask:0xf
	v_mov_b32_e32 v31, v69
	v_accvgpr_read_b32 v14, a16
	v_accvgpr_read_b32 v28, a46
	v_pk_add_f32 v[60:61], v[60:61], v[62:63]
	v_pk_mul_f32 v[62:63], v[30:31], v[44:45]
	v_accvgpr_read_b32 v15, a17
	v_accvgpr_read_b32 v29, a47
	v_mov_b32_dpp v39, v68 row_shl:1 row_mask:0xf bank_mask:0xf
	v_pk_fma_f32 v[62:63], v[68:69], v[14:15], v[62:63] op_sel_hi:[0,1,1]
	v_pk_mov_b32 v[68:69], v[68:69], v[28:29] op_sel:[1,0]
	v_mov_b32_e32 v36, v25
	v_pk_fma_f32 v[62:63], v[68:69], v[38:39], v[62:63]
	s_mov_b64 s[0:1], 0x1400000
	v_pk_add_f32 v[60:61], v[60:61], v[62:63]
	v_mov_b32_dpp v36, v71 row_shr:1 row_mask:0xf bank_mask:0xf
	v_mov_b32_e32 v127, v71
	v_accvgpr_read_b32 v8, a20
	v_lshl_add_u64 v[62:63], v[54:55], 0, s[0:1]
	v_mov_b32_e32 v128, v60
	v_mov_b32_e32 v129, v61
	v_pk_mul_f32 v[60:61], v[126:127], v[36:37]
	v_accvgpr_read_b32 v9, a21
	v_accvgpr_write_b32 a25, v23
	v_mov_b32_e32 v12, v7
	v_mov_b32_dpp v25, v70 row_shl:1 row_mask:0xf bank_mask:0xf
	v_pk_fma_f32 v[60:61], v[70:71], v[8:9], v[60:61] op_sel_hi:[0,1,1]
	v_mov_b32_e32 v62, v71
	v_mov_b32_e32 v63, v101
	v_accvgpr_write_b32 a24, v22
	v_mov_b32_dpp v12, v73 row_shr:1 row_mask:0xf bank_mask:0xf
	v_mov_b32_e32 v74, v52
	v_mov_b32_e32 v75, v73
	v_accvgpr_read_b32 v23, a9
	v_accvgpr_write_b32 a26, v124
	v_accvgpr_mov_b32 a2, a22
	v_pk_fma_f32 v[60:61], v[62:63], v[24:25], v[60:61]
	v_pk_mul_f32 v[62:63], v[74:75], v[12:13]
	v_accvgpr_read_b32 v22, a8
	v_accvgpr_write_b32 a27, v125
	v_accvgpr_mov_b32 a3, a23
	v_accvgpr_write_b32 a22, v88
	v_mov_b32_dpp v7, v72 row_shl:1 row_mask:0xf bank_mask:0xf
	v_pk_fma_f32 v[62:63], v[72:73], v[22:23], v[62:63] op_sel_hi:[0,1,1]
	v_mov_b32_e32 v68, v73
	v_mov_b32_e32 v69, v67
	v_mov_b32_e32 v78, v21
	v_accvgpr_write_b32 a23, v89
	v_pk_fma_f32 v[62:63], v[68:69], v[6:7], v[62:63]
	v_pk_add_f32 v[60:61], v[60:61], 0 op_sel_hi:[1,0]
	v_mov_b32_dpp v78, v83 row_shr:1 row_mask:0xf bank_mask:0xf
	v_accvgpr_read_b32 v52, a30
	v_mov_b32_e32 v53, v83
	v_accvgpr_read_b32 v89, a27
	v_pk_add_f32 v[60:61], v[60:61], v[62:63]
	v_pk_mul_f32 v[62:63], v[52:53], v[78:79]
	v_accvgpr_read_b32 v88, a26
	v_mov_b32_dpp v21, v82 row_shl:1 row_mask:0xf bank_mask:0xf
	v_pk_fma_f32 v[62:63], v[82:83], v[88:89], v[62:63] op_sel_hi:[0,1,1]
	v_mov_b32_e32 v68, v83
	v_mov_b32_e32 v69, v29
	v_pk_fma_f32 v[62:63], v[68:69], v[20:21], v[62:63]
	v_mov_b32_e32 v76, v11
	v_accvgpr_read_b32 v125, a37
	v_pk_add_f32 v[60:61], v[60:61], v[62:63]
	s_mov_b64 s[0:1], 0x1410000
	v_mov_b32_dpp v76, v81 row_shr:1 row_mask:0xf bank_mask:0xf
	v_mov_b32_e32 v121, v81
	v_accvgpr_read_b32 v101, a15
	v_accvgpr_read_b32 v124, a36
	v_lshl_add_u64 v[136:137], v[134:135], 0, s[0:1]
	s_nop 1
	s_mov_b64 vcc, s[28:29]
	s_nop 0
	v_cndmask_b32_dpp v130, v60, v128, vcc quad_perm:[1,0,3,2] row_mask:0xf bank_mask:0xf
	v_cndmask_b32_dpp v131, v61, v129, vcc quad_perm:[1,0,3,2] row_mask:0xf bank_mask:0xf
	s_mov_b64 vcc, s[30:31]
	s_nop 0
	v_cndmask_b32_dpp v132, v128, v60, vcc quad_perm:[1,0,3,2] row_mask:0xf bank_mask:0xf
	v_cndmask_b32_dpp v133, v129, v61, vcc quad_perm:[1,0,3,2] row_mask:0xf bank_mask:0xf
	global_store_dwordx4 v[136:137], v[130:133], off sc0 sc1 nt
	s_nop 1
	v_pk_mul_f32 v[60:61], v[120:121], v[76:77]
	v_accvgpr_read_b32 v100, a14
	v_mov_b32_e32 v2, v35
	v_mov_b32_dpp v11, v80 row_shl:1 row_mask:0xf bank_mask:0xf
	v_pk_fma_f32 v[60:61], v[80:81], v[124:125], v[60:61] op_sel_hi:[0,1,1]
	v_pk_mov_b32 v[62:63], v[80:81], v[100:101] op_sel:[1,0]
	v_mov_b32_dpp v2, v85 row_shr:1 row_mask:0xf bank_mask:0xf
	v_mov_b32_e32 v107, v85
	v_accvgpr_read_b32 v29, a13
	v_pk_fma_f32 v[60:61], v[62:63], v[10:11], v[60:61]
	v_pk_mul_f32 v[62:63], v[106:107], v[2:3]
	v_accvgpr_read_b32 v28, a12
	v_mov_b32_dpp v35, v84 row_shl:1 row_mask:0xf bank_mask:0xf
	v_pk_fma_f32 v[62:63], v[84:85], v[28:29], v[62:63] op_sel_hi:[0,1,1]
	v_pk_mov_b32 v[68:69], v[84:85], v[122:123] op_sel:[1,0]
	v_mov_b32_e32 v92, v59
	v_pk_fma_f32 v[62:63], v[68:69], v[34:35], v[62:63]
	v_pk_add_f32 v[60:61], v[60:61], 0 op_sel_hi:[1,0]
	v_mov_b32_dpp v92, v117 row_shr:1 row_mask:0xf bank_mask:0xf
	v_mov_b32_e32 v97, v117
	v_pk_add_f32 v[60:61], v[60:61], v[62:63]
	v_pk_mul_f32 v[62:63], v[96:97], v[92:93]
	v_accvgpr_write_b32 a8, v118
	v_pk_fma_f32 v[62:63], v[116:117], v[118:119], v[62:63] op_sel_hi:[0,1,1]
	v_accvgpr_write_b32 a9, v119
	v_accvgpr_read_b32 v119, a45
	v_accvgpr_read_b32 v118, a44
	v_mov_b32_dpp v59, v116 row_shl:1 row_mask:0xf bank_mask:0xf
	v_pk_mov_b32 v[68:69], v[116:117], v[118:119] op_sel:[1,0]
	v_mov_b32_e32 v94, v57
	v_pk_fma_f32 v[62:63], v[68:69], v[58:59], v[62:63]
	s_mov_b64 s[0:1], 0x1420000
	v_pk_add_f32 v[60:61], v[60:61], v[62:63]
	v_mov_b32_dpp v94, v115 row_shr:1 row_mask:0xf bank_mask:0xf
	v_mov_b32_e32 v99, v115
	v_accvgpr_read_b32 v41, a11
	v_lshl_add_u64 v[62:63], v[54:55], 0, s[0:1]
	v_mov_b32_e32 v128, v60
	v_mov_b32_e32 v129, v61
	v_pk_mul_f32 v[60:61], v[98:99], v[94:95]
	v_accvgpr_read_b32 v40, a10
	v_mov_b32_e32 v102, v51
	v_mov_b32_dpp v57, v114 row_shl:1 row_mask:0xf bank_mask:0xf
	v_pk_fma_f32 v[60:61], v[114:115], v[40:41], v[60:61] op_sel_hi:[0,1,1]
	v_mov_b32_e32 v62, v115
	v_mov_b32_e32 v63, v101
	v_mov_b32_dpp v102, v113 row_shr:1 row_mask:0xf bank_mask:0xf
	v_mov_b32_e32 v105, v113
	v_pk_fma_f32 v[60:61], v[62:63], v[56:57], v[60:61]
	v_pk_mul_f32 v[62:63], v[104:105], v[102:103]
	v_mov_b32_dpp v51, v112 row_shl:1 row_mask:0xf bank_mask:0xf
	v_pk_fma_f32 v[62:63], v[112:113], v[4:5], v[62:63] op_sel_hi:[0,1,1]
	v_mov_b32_e32 v68, v113
	v_mov_b32_e32 v69, v123
	v_mov_b32_e32 v108, v49
	v_pk_fma_f32 v[62:63], v[68:69], v[50:51], v[62:63]
	v_pk_add_f32 v[60:61], v[60:61], 0 op_sel_hi:[1,0]
	v_mov_b32_dpp v108, v91 row_shr:1 row_mask:0xf bank_mask:0xf
	v_mov_b32_e32 v111, v91
	v_accvgpr_read_b32 v5, a3
	v_pk_add_f32 v[60:61], v[60:61], v[62:63]
	v_pk_mul_f32 v[62:63], v[110:111], v[108:109]
	v_accvgpr_read_b32 v4, a2
	v_mov_b32_dpp v49, v90 row_shl:1 row_mask:0xf bank_mask:0xf
	v_pk_fma_f32 v[62:63], v[90:91], v[4:5], v[62:63] op_sel_hi:[0,1,1]
	v_mov_b32_e32 v68, v91
	v_mov_b32_e32 v69, v119
	v_pk_fma_f32 v[62:63], v[68:69], v[48:49], v[62:63]
	s_mov_b64 s[0:1], 0x1430000
	v_pk_add_f32 v[60:61], v[60:61], v[62:63]
	v_lshl_add_u64 v[136:137], v[134:135], 0, s[0:1]
	s_nop 1
	s_mov_b64 vcc, s[28:29]
	s_nop 0
	v_cndmask_b32_dpp v130, v60, v128, vcc quad_perm:[1,0,3,2] row_mask:0xf bank_mask:0xf
	v_cndmask_b32_dpp v131, v61, v129, vcc quad_perm:[1,0,3,2] row_mask:0xf bank_mask:0xf
	s_mov_b64 vcc, s[30:31]
	s_nop 0
	v_cndmask_b32_dpp v132, v128, v60, vcc quad_perm:[1,0,3,2] row_mask:0xf bank_mask:0xf
	v_cndmask_b32_dpp v133, v129, v61, vcc quad_perm:[1,0,3,2] row_mask:0xf bank_mask:0xf
	global_store_dwordx4 v[136:137], v[130:133], off sc0 sc1 nt
	s_nop 1
	s_waitcnt vmcnt(12)
	s_waitcnt lgkmcnt(0)
	s_barrier
	v_accvgpr_read_b32 v2, a1
	v_accvgpr_read_b32 v12, a5
	ds_read_b64 v[60:61], v12
	ds_read_b64 v[62:63], v12 offset:288
	ds_read_b64 v[68:69], v12 offset:576
	ds_read_b64 v[70:71], v12 offset:1728
	ds_read_b64 v[72:73], v12 offset:2016
	ds_read_b64 v[82:83], v12 offset:2304
	ds_read_b64 v[80:81], v12 offset:3456
	ds_read_b64 v[84:85], v12 offset:3744
	ds_read_b64 v[116:117], v12 offset:4032
	ds_read_b64 v[114:115], v12 offset:5184
	ds_read_b64 v[112:113], v12 offset:5472
	ds_read_b64 v[90:91], v12 offset:5760
	ds_read_b32 v43, v2
	ds_read_b32 v19, v2 offset:288
	ds_read_b32 v39, v2 offset:576
	ds_read_b32 v25, v2 offset:1728
	ds_read_b32 v7, v2 offset:2016
	ds_read_b32 v21, v2 offset:2304
	ds_read_b32 v11, v2 offset:3456
	ds_read_b32 v35, v2 offset:3744
	ds_read_b32 v59, v2 offset:4032
	ds_read_b32 v57, v2 offset:5184
	ds_read_b32 v51, v2 offset:5472
	ds_read_b32 v49, v2 offset:5760
	s_waitcnt lgkmcnt(0)
	v_accvgpr_read_b32 v101, a23
	v_mov_b32_e32 v46, v43
	v_mov_b32_e32 v65, v61
	v_accvgpr_read_b32 v31, a25
	v_mov_b32_dpp v46, v61 row_shr:1 row_mask:0xf bank_mask:0xf
	v_pk_mul_f32 v[86:87], v[64:65], v[46:47]
	v_accvgpr_read_b32 v100, a22
	v_accvgpr_read_b32 v30, a24
	v_mov_b32_e32 v26, v19
	v_mov_b32_dpp v43, v60 row_shl:1 row_mask:0xf bank_mask:0xf
	v_pk_fma_f32 v[86:87], v[60:61], v[100:101], v[86:87] op_sel_hi:[0,1,1]
	v_pk_mov_b32 v[60:61], v[60:61], v[30:31] op_sel:[1,0]
	v_mov_b32_dpp v26, v63 row_shr:1 row_mask:0xf bank_mask:0xf
	v_mov_b32_e32 v1, v63
	v_pk_fma_f32 v[60:61], v[60:61], v[42:43], v[86:87]
	v_pk_mul_f32 v[86:87], v[0:1], v[26:27]
	v_accvgpr_read_b32 v0, a34
	v_accvgpr_mov_b32 a12, a14
	v_accvgpr_read_b32 v1, a35
	v_accvgpr_mov_b32 a13, a15
	v_mov_b32_dpp v19, v62 row_shl:1 row_mask:0xf bank_mask:0xf
	v_pk_fma_f32 v[86:87], v[62:63], v[16:17], v[86:87] op_sel_hi:[0,1,1]
	v_accvgpr_write_b32 a14, v16
	v_pk_mov_b32 v[62:63], v[62:63], v[0:1] op_sel:[1,0]
	v_mov_b32_e32 v44, v39
	v_accvgpr_write_b32 a15, v17
	v_pk_fma_f32 v[62:63], v[62:63], v[18:19], v[86:87]
	v_pk_add_f32 v[60:61], v[60:61], 0 op_sel_hi:[1,0]
	v_mov_b32_dpp v44, v69 row_shr:1 row_mask:0xf bank_mask:0xf
	v_accvgpr_read_b32 v16, a48
	v_mov_b32_e32 v17, v69
	v_accvgpr_read_b32 v67, a47
	v_pk_add_f32 v[60:61], v[60:61], v[62:63]
	v_pk_mul_f32 v[62:63], v[16:17], v[44:45]
	v_accvgpr_read_b32 v66, a46
	v_mov_b32_dpp v39, v68 row_shl:1 row_mask:0xf bank_mask:0xf
	v_pk_fma_f32 v[62:63], v[68:69], v[14:15], v[62:63] op_sel_hi:[0,1,1]
	v_pk_mov_b32 v[68:69], v[68:69], v[66:67] op_sel:[1,0]
	v_mov_b32_e32 v36, v25
	v_pk_fma_f32 v[62:63], v[68:69], v[38:39], v[62:63]
	s_mov_b64 s[0:1], 0x1800000
	v_pk_add_f32 v[60:61], v[60:61], v[62:63]
	v_mov_b32_dpp v36, v71 row_shr:1 row_mask:0xf bank_mask:0xf
	v_mov_b32_e32 v127, v71
	v_lshl_add_u64 v[62:63], v[54:55], 0, s[0:1]
	v_mov_b32_e32 v128, v60
	v_mov_b32_e32 v129, v61
	v_pk_mul_f32 v[60:61], v[126:127], v[36:37]
	v_mov_b32_e32 v12, v7
	v_mov_b32_dpp v25, v70 row_shl:1 row_mask:0xf bank_mask:0xf
	v_pk_fma_f32 v[60:61], v[70:71], v[8:9], v[60:61] op_sel_hi:[0,1,1]
	v_mov_b32_e32 v62, v71
	v_mov_b32_e32 v63, v31
	v_mov_b32_dpp v12, v73 row_shr:1 row_mask:0xf bank_mask:0xf
	v_mov_b32_e32 v75, v73
	v_pk_fma_f32 v[60:61], v[62:63], v[24:25], v[60:61]
	v_pk_mul_f32 v[62:63], v[74:75], v[12:13]
	v_mov_b32_dpp v7, v72 row_shl:1 row_mask:0xf bank_mask:0xf
	v_pk_fma_f32 v[62:63], v[72:73], v[22:23], v[62:63] op_sel_hi:[0,1,1]
	v_accvgpr_write_b32 a4, v22
	v_mov_b32_e32 v68, v73
	v_mov_b32_e32 v69, v1
	v_mov_b32_e32 v78, v21
	v_accvgpr_write_b32 a5, v23
	v_pk_fma_f32 v[62:63], v[68:69], v[6:7], v[62:63]
	v_pk_add_f32 v[60:61], v[60:61], 0 op_sel_hi:[1,0]
	v_mov_b32_dpp v78, v83 row_shr:1 row_mask:0xf bank_mask:0xf
	v_mov_b32_e32 v53, v83
	v_accvgpr_read_b32 v22, a26
	v_pk_add_f32 v[60:61], v[60:61], v[62:63]
	v_pk_mul_f32 v[62:63], v[52:53], v[78:79]
	v_accvgpr_read_b32 v23, a27
	v_mov_b32_dpp v21, v82 row_shl:1 row_mask:0xf bank_mask:0xf
	v_pk_fma_f32 v[62:63], v[82:83], v[22:23], v[62:63] op_sel_hi:[0,1,1]
	v_mov_b32_e32 v68, v83
	v_mov_b32_e32 v69, v67
	v_pk_fma_f32 v[62:63], v[68:69], v[20:21], v[62:63]
	v_mov_b32_e32 v76, v11
	v_pk_add_f32 v[60:61], v[60:61], v[62:63]
	s_mov_b64 s[0:1], 0x1810000
	v_mov_b32_dpp v76, v81 row_shr:1 row_mask:0xf bank_mask:0xf
	v_mov_b32_e32 v121, v81
	v_accvgpr_read_b32 v15, a13
	v_lshl_add_u64 v[136:137], v[134:135], 0, s[0:1]
	s_nop 1
	s_mov_b64 vcc, s[28:29]
	s_nop 0
	v_cndmask_b32_dpp v130, v60, v128, vcc quad_perm:[1,0,3,2] row_mask:0xf bank_mask:0xf
	v_cndmask_b32_dpp v131, v61, v129, vcc quad_perm:[1,0,3,2] row_mask:0xf bank_mask:0xf
	s_mov_b64 vcc, s[30:31]
	s_nop 0
	v_cndmask_b32_dpp v132, v128, v60, vcc quad_perm:[1,0,3,2] row_mask:0xf bank_mask:0xf
	v_cndmask_b32_dpp v133, v129, v61, vcc quad_perm:[1,0,3,2] row_mask:0xf bank_mask:0xf
	global_store_dwordx4 v[136:137], v[130:133], off sc0 sc1 nt
	s_nop 1
	v_pk_mul_f32 v[60:61], v[120:121], v[76:77]
	v_accvgpr_read_b32 v14, a12
	v_mov_b32_e32 v2, v35
	v_mov_b32_dpp v11, v80 row_shl:1 row_mask:0xf bank_mask:0xf
	v_pk_fma_f32 v[60:61], v[80:81], v[124:125], v[60:61] op_sel_hi:[0,1,1]
	v_pk_mov_b32 v[62:63], v[80:81], v[14:15] op_sel:[1,0]
	v_mov_b32_dpp v2, v85 row_shr:1 row_mask:0xf bank_mask:0xf
	v_mov_b32_e32 v107, v85
	v_pk_fma_f32 v[60:61], v[62:63], v[10:11], v[60:61]
	v_pk_mul_f32 v[62:63], v[106:107], v[2:3]
	v_mov_b32_dpp v35, v84 row_shl:1 row_mask:0xf bank_mask:0xf
	v_pk_fma_f32 v[62:63], v[84:85], v[28:29], v[62:63] op_sel_hi:[0,1,1]
	v_pk_mov_b32 v[68:69], v[84:85], v[122:123] op_sel:[1,0]
	v_mov_b32_e32 v92, v59
	v_pk_fma_f32 v[62:63], v[68:69], v[34:35], v[62:63]
	v_pk_add_f32 v[60:61], v[60:61], 0 op_sel_hi:[1,0]
	v_mov_b32_dpp v92, v117 row_shr:1 row_mask:0xf bank_mask:0xf
	v_mov_b32_e32 v97, v117
	v_accvgpr_read_b32 v87, a9
	v_pk_add_f32 v[60:61], v[60:61], v[62:63]
	v_pk_mul_f32 v[62:63], v[96:97], v[92:93]
	v_accvgpr_read_b32 v86, a8
	v_mov_b32_dpp v59, v116 row_shl:1 row_mask:0xf bank_mask:0xf
	v_pk_fma_f32 v[62:63], v[116:117], v[86:87], v[62:63] op_sel_hi:[0,1,1]
	v_pk_mov_b32 v[68:69], v[116:117], v[118:119] op_sel:[1,0]
	v_mov_b32_e32 v94, v57
	v_pk_fma_f32 v[62:63], v[68:69], v[58:59], v[62:63]
	s_mov_b64 s[0:1], 0x1820000
	v_pk_add_f32 v[60:61], v[60:61], v[62:63]
	v_mov_b32_dpp v94, v115 row_shr:1 row_mask:0xf bank_mask:0xf
	v_mov_b32_e32 v99, v115
	v_lshl_add_u64 v[62:63], v[54:55], 0, s[0:1]
	v_mov_b32_e32 v128, v60
	v_mov_b32_e32 v129, v61
	v_pk_mul_f32 v[60:61], v[98:99], v[94:95]
	v_mov_b32_e32 v102, v51
	v_mov_b32_dpp v57, v114 row_shl:1 row_mask:0xf bank_mask:0xf
	v_pk_fma_f32 v[60:61], v[114:115], v[40:41], v[60:61] op_sel_hi:[0,1,1]
	v_mov_b32_e32 v62, v115
	v_mov_b32_e32 v63, v15
	v_mov_b32_dpp v102, v113 row_shr:1 row_mask:0xf bank_mask:0xf
	v_mov_b32_e32 v105, v113
	v_accvgpr_read_b32 v89, a19
	v_pk_fma_f32 v[60:61], v[62:63], v[56:57], v[60:61]
	v_pk_mul_f32 v[62:63], v[104:105], v[102:103]
	v_accvgpr_read_b32 v88, a18
	v_mov_b32_dpp v51, v112 row_shl:1 row_mask:0xf bank_mask:0xf
	v_pk_fma_f32 v[62:63], v[112:113], v[88:89], v[62:63] op_sel_hi:[0,1,1]
	v_mov_b32_e32 v68, v113
	v_mov_b32_e32 v69, v123
	v_mov_b32_e32 v108, v49
	v_pk_fma_f32 v[62:63], v[68:69], v[50:51], v[62:63]
	v_pk_add_f32 v[60:61], v[60:61], 0 op_sel_hi:[1,0]
	v_mov_b32_dpp v108, v91 row_shr:1 row_mask:0xf bank_mask:0xf
	v_mov_b32_e32 v111, v91
	v_pk_add_f32 v[60:61], v[60:61], v[62:63]
	v_pk_mul_f32 v[62:63], v[110:111], v[108:109]
	v_mov_b32_dpp v49, v90 row_shl:1 row_mask:0xf bank_mask:0xf
	v_pk_fma_f32 v[62:63], v[90:91], v[4:5], v[62:63] op_sel_hi:[0,1,1]
	v_mov_b32_e32 v68, v91
	v_mov_b32_e32 v69, v119
	v_pk_fma_f32 v[62:63], v[68:69], v[48:49], v[62:63]
	s_mov_b64 s[0:1], 0x1830000
	v_pk_add_f32 v[60:61], v[60:61], v[62:63]
	v_lshl_add_u64 v[136:137], v[134:135], 0, s[0:1]
	s_nop 1
	s_mov_b64 vcc, s[28:29]
	s_nop 0
	v_cndmask_b32_dpp v130, v60, v128, vcc quad_perm:[1,0,3,2] row_mask:0xf bank_mask:0xf
	v_cndmask_b32_dpp v131, v61, v129, vcc quad_perm:[1,0,3,2] row_mask:0xf bank_mask:0xf
	s_mov_b64 vcc, s[30:31]
	s_nop 0
	v_cndmask_b32_dpp v132, v128, v60, vcc quad_perm:[1,0,3,2] row_mask:0xf bank_mask:0xf
	v_cndmask_b32_dpp v133, v129, v61, vcc quad_perm:[1,0,3,2] row_mask:0xf bank_mask:0xf
	global_store_dwordx4 v[136:137], v[130:133], off sc0 sc1 nt
	s_nop 1
	v_accvgpr_write_b32 a12, v28
	s_waitcnt vmcnt(8)
	v_accvgpr_write_b32 a13, v29
	v_mov_b64_e32 v[28:29], v[4:5]
	s_waitcnt lgkmcnt(0)
	s_barrier
	v_accvgpr_read_b32 v2, a6
	v_accvgpr_read_b32 v4, a7
	ds_read_b64 v[60:61], v2
	ds_read_b64 v[62:63], v2 offset:288
	ds_read_b64 v[68:69], v2 offset:576
	ds_read_b64 v[70:71], v2 offset:1728
	ds_read_b64 v[72:73], v2 offset:2016
	ds_read_b64 v[82:83], v2 offset:2304
	ds_read_b64 v[80:81], v2 offset:3456
	ds_read_b64 v[84:85], v2 offset:3744
	ds_read_b64 v[116:117], v2 offset:4032
	ds_read_b64 v[114:115], v2 offset:5184
	ds_read_b64 v[112:113], v2 offset:5472
	ds_read_b64 v[90:91], v2 offset:5760
	ds_read_b32 v43, v4
	ds_read_b32 v19, v4 offset:288
	ds_read_b32 v39, v4 offset:576
	ds_read_b32 v25, v4 offset:1728
	ds_read_b32 v7, v4 offset:2016
	ds_read_b32 v21, v4 offset:2304
	ds_read_b32 v11, v4 offset:3456
	ds_read_b32 v35, v4 offset:3744
	ds_read_b32 v59, v4 offset:4032
	ds_read_b32 v57, v4 offset:5184
	ds_read_b32 v51, v4 offset:5472
	ds_read_b32 v49, v4 offset:5760
	s_waitcnt lgkmcnt(0)
	v_accvgpr_read_b32 v8, a24
	v_mov_b32_e32 v46, v43
	v_mov_b32_e32 v65, v61
	v_mov_b32_e32 v26, v19
	v_mov_b32_dpp v46, v61 row_shr:1 row_mask:0xf bank_mask:0xf
	v_accvgpr_read_b32 v32, a32
	v_accvgpr_read_b32 v9, a25
	v_mov_b64_e32 v[124:125], v[40:41]
	v_pk_mul_f32 v[30:31], v[64:65], v[46:47]
	v_mov_b32_dpp v26, v63 row_shr:1 row_mask:0xf bank_mask:0xf
	v_mov_b32_e32 v33, v63
	v_accvgpr_read_b32 v4, a14
	v_accvgpr_read_b32 v41, a35
	v_mov_b32_e32 v44, v39
	v_pk_fma_f32 v[30:31], v[60:61], v[100:101], v[30:31] op_sel_hi:[0,1,1]
	v_mov_b32_dpp v43, v60 row_shl:1 row_mask:0xf bank_mask:0xf
	v_pk_mov_b32 v[46:47], v[60:61], v[8:9] op_sel:[1,0]
	v_pk_mul_f32 v[26:27], v[32:33], v[26:27]
	v_accvgpr_read_b32 v5, a15
	v_accvgpr_read_b32 v40, a34
	v_mov_b32_dpp v44, v69 row_shr:1 row_mask:0xf bank_mask:0xf
	v_mov_b32_e32 v17, v69
	v_accvgpr_read_b32 v0, a16
	v_pk_fma_f32 v[30:31], v[46:47], v[42:43], v[30:31]
	v_pk_fma_f32 v[26:27], v[62:63], v[4:5], v[26:27] op_sel_hi:[0,1,1]
	v_mov_b32_dpp v19, v62 row_shl:1 row_mask:0xf bank_mask:0xf
	v_pk_mov_b32 v[32:33], v[62:63], v[40:41] op_sel:[1,0]
	v_pk_mul_f32 v[16:17], v[16:17], v[44:45]
	v_accvgpr_read_b32 v1, a17
	v_pk_fma_f32 v[18:19], v[32:33], v[18:19], v[26:27]
	v_pk_add_f32 v[26:27], v[30:31], 0 op_sel_hi:[1,0]
	v_mov_b32_dpp v39, v68 row_shl:1 row_mask:0xf bank_mask:0xf
	v_pk_fma_f32 v[16:17], v[68:69], v[0:1], v[16:17] op_sel_hi:[0,1,1]
	v_pk_mov_b32 v[30:31], v[68:69], v[66:67] op_sel:[1,0]
	v_pk_add_f32 v[18:19], v[26:27], v[18:19]
	v_pk_fma_f32 v[16:17], v[30:31], v[38:39], v[16:17]
	v_mov_b32_e32 v36, v25
	s_mov_b64 s[0:1], 0x1c00000
	v_pk_add_f32 v[16:17], v[18:19], v[16:17]
	v_mov_b32_dpp v36, v71 row_shr:1 row_mask:0xf bank_mask:0xf
	v_mov_b32_e32 v127, v71
	v_accvgpr_read_b32 v0, a20
	v_lshl_add_u64 v[26:27], v[54:55], 0, s[0:1]
	v_mov_b32_e32 v128, v16
	v_mov_b32_e32 v129, v17
	v_mov_b32_e32 v12, v7
	v_pk_mul_f32 v[16:17], v[126:127], v[36:37]
	v_accvgpr_read_b32 v1, a21
	v_mov_b32_dpp v12, v73 row_shr:1 row_mask:0xf bank_mask:0xf
	v_pk_fma_f32 v[16:17], v[70:71], v[0:1], v[16:17] op_sel_hi:[0,1,1]
	v_mov_b32_e32 v75, v73
	v_accvgpr_read_b32 v0, a4
	v_mov_b32_e32 v78, v21
	v_pk_mul_f32 v[12:13], v[74:75], v[12:13]
	v_accvgpr_read_b32 v1, a5
	v_mov_b32_dpp v25, v70 row_shl:1 row_mask:0xf bank_mask:0xf
	v_mov_b32_dpp v7, v72 row_shl:1 row_mask:0xf bank_mask:0xf
	v_mov_b32_dpp v78, v83 row_shr:1 row_mask:0xf bank_mask:0xf
	v_mov_b32_e32 v8, v71
	v_pk_fma_f32 v[12:13], v[72:73], v[0:1], v[12:13] op_sel_hi:[0,1,1]
	v_mov_b32_e32 v5, v41
	v_mov_b32_e32 v4, v73
	v_mov_b32_e32 v53, v83
	v_pk_fma_f32 v[16:17], v[8:9], v[24:25], v[16:17]
	v_pk_fma_f32 v[6:7], v[4:5], v[6:7], v[12:13]
	v_pk_mul_f32 v[12:13], v[52:53], v[78:79]
	v_mov_b32_dpp v21, v82 row_shl:1 row_mask:0xf bank_mask:0xf
	v_pk_add_f32 v[16:17], v[16:17], 0 op_sel_hi:[1,0]
	v_pk_fma_f32 v[12:13], v[82:83], v[22:23], v[12:13] op_sel_hi:[0,1,1]
	v_mov_b32_e32 v66, v83
	v_pk_add_f32 v[6:7], v[16:17], v[6:7]
	v_pk_fma_f32 v[12:13], v[66:67], v[20:21], v[12:13]
	v_mov_b32_e32 v76, v11
	v_pk_add_f32 v[6:7], v[6:7], v[12:13]
	s_mov_b64 s[0:1], 0x1c10000
	v_mov_b32_dpp v76, v81 row_shr:1 row_mask:0xf bank_mask:0xf
	v_mov_b32_e32 v121, v81
	v_accvgpr_read_b32 v0, a36
	v_lshl_add_u64 v[136:137], v[134:135], 0, s[0:1]
	s_nop 1
	s_mov_b64 vcc, s[28:29]
	s_nop 0
	v_cndmask_b32_dpp v130, v6, v128, vcc quad_perm:[1,0,3,2] row_mask:0xf bank_mask:0xf
	v_cndmask_b32_dpp v131, v7, v129, vcc quad_perm:[1,0,3,2] row_mask:0xf bank_mask:0xf
	s_mov_b64 vcc, s[30:31]
	s_nop 0
	v_cndmask_b32_dpp v132, v128, v6, vcc quad_perm:[1,0,3,2] row_mask:0xf bank_mask:0xf
	v_cndmask_b32_dpp v133, v129, v7, vcc quad_perm:[1,0,3,2] row_mask:0xf bank_mask:0xf
	global_store_dwordx4 v[136:137], v[130:133], off sc0 sc1 nt
	s_nop 1
	v_mov_b32_e32 v2, v35
	v_pk_mul_f32 v[6:7], v[120:121], v[76:77]
	v_accvgpr_read_b32 v1, a37
	v_mov_b32_dpp v2, v85 row_shr:1 row_mask:0xf bank_mask:0xf
	v_pk_fma_f32 v[6:7], v[80:81], v[0:1], v[6:7] op_sel_hi:[0,1,1]
	v_mov_b32_e32 v107, v85
	v_accvgpr_read_b32 v0, a12
	v_mov_b32_e32 v92, v59
	v_pk_mul_f32 v[2:3], v[106:107], v[2:3]
	v_accvgpr_read_b32 v1, a13
	v_mov_b32_dpp v11, v80 row_shl:1 row_mask:0xf bank_mask:0xf
	v_mov_b32_dpp v35, v84 row_shl:1 row_mask:0xf bank_mask:0xf
	v_mov_b32_dpp v92, v117 row_shr:1 row_mask:0xf bank_mask:0xf
	v_pk_mov_b32 v[8:9], v[80:81], v[14:15] op_sel:[1,0]
	v_pk_fma_f32 v[2:3], v[84:85], v[0:1], v[2:3] op_sel_hi:[0,1,1]
	v_pk_mov_b32 v[4:5], v[84:85], v[122:123] op_sel:[1,0]
	v_mov_b32_e32 v97, v117
	v_pk_fma_f32 v[6:7], v[8:9], v[10:11], v[6:7]
	v_pk_fma_f32 v[0:1], v[4:5], v[34:35], v[2:3]
	v_pk_mul_f32 v[2:3], v[96:97], v[92:93]
	v_mov_b32_dpp v59, v116 row_shl:1 row_mask:0xf bank_mask:0xf
	v_pk_add_f32 v[6:7], v[6:7], 0 op_sel_hi:[1,0]
	v_pk_fma_f32 v[2:3], v[116:117], v[86:87], v[2:3] op_sel_hi:[0,1,1]
	v_pk_mov_b32 v[4:5], v[116:117], v[118:119] op_sel:[1,0]
	v_pk_add_f32 v[0:1], v[6:7], v[0:1]
	v_pk_fma_f32 v[2:3], v[4:5], v[58:59], v[2:3]
	v_mov_b32_e32 v94, v57
	v_pk_add_f32 v[0:1], v[0:1], v[2:3]
	s_mov_b64 s[0:1], 0x1c20000
	v_mov_b32_dpp v94, v115 row_shr:1 row_mask:0xf bank_mask:0xf
	v_mov_b32_e32 v102, v51
	v_mov_b32_e32 v99, v115
	v_lshl_add_u64 v[2:3], v[54:55], 0, s[0:1]
	v_mov_b32_e32 v128, v0
	v_mov_b32_e32 v129, v1
	v_mov_b32_dpp v102, v113 row_shr:1 row_mask:0xf bank_mask:0xf
	v_pk_mul_f32 v[0:1], v[98:99], v[94:95]
	v_mov_b32_e32 v105, v113
	v_mov_b32_dpp v57, v114 row_shl:1 row_mask:0xf bank_mask:0xf
	v_pk_fma_f32 v[0:1], v[114:115], v[124:125], v[0:1] op_sel_hi:[0,1,1]
	v_mov_b32_e32 v14, v115
	v_pk_mul_f32 v[2:3], v[104:105], v[102:103]
	v_mov_b32_dpp v51, v112 row_shl:1 row_mask:0xf bank_mask:0xf
	v_mov_b32_e32 v108, v49
	v_pk_fma_f32 v[0:1], v[14:15], v[56:57], v[0:1]
	v_pk_fma_f32 v[2:3], v[112:113], v[88:89], v[2:3] op_sel_hi:[0,1,1]
	v_mov_b32_e32 v122, v113
	v_mov_b32_dpp v108, v91 row_shr:1 row_mask:0xf bank_mask:0xf
	v_pk_add_f32 v[0:1], v[0:1], 0 op_sel_hi:[1,0]
	v_pk_fma_f32 v[2:3], v[122:123], v[50:51], v[2:3]
	v_mov_b32_e32 v111, v91
	v_pk_add_f32 v[0:1], v[0:1], v[2:3]
	v_pk_mul_f32 v[2:3], v[110:111], v[108:109]
	v_mov_b32_dpp v49, v90 row_shl:1 row_mask:0xf bank_mask:0xf
	v_pk_fma_f32 v[2:3], v[90:91], v[28:29], v[2:3] op_sel_hi:[0,1,1]
	v_mov_b32_e32 v118, v91
	v_pk_fma_f32 v[2:3], v[118:119], v[48:49], v[2:3]
	s_mov_b64 s[0:1], 0x1c30000
	v_pk_add_f32 v[0:1], v[0:1], v[2:3]
	v_lshl_add_u64 v[136:137], v[134:135], 0, s[0:1]
	s_nop 1
	s_mov_b64 vcc, s[28:29]
	s_nop 0
	v_cndmask_b32_dpp v130, v0, v128, vcc quad_perm:[1,0,3,2] row_mask:0xf bank_mask:0xf
	v_cndmask_b32_dpp v131, v1, v129, vcc quad_perm:[1,0,3,2] row_mask:0xf bank_mask:0xf
	s_mov_b64 vcc, s[30:31]
	s_nop 0
	v_cndmask_b32_dpp v132, v128, v0, vcc quad_perm:[1,0,3,2] row_mask:0xf bank_mask:0xf
	v_cndmask_b32_dpp v133, v129, v1, vcc quad_perm:[1,0,3,2] row_mask:0xf bank_mask:0xf
	global_store_dwordx4 v[136:137], v[130:133], off sc0 sc1 nt
	s_nop 1
	s_endpgm
